# E6 + MoE grouped GEMMs skip the 32-MFMA blocks of a wave's 64-row slab when the slab is entirely padding (rows >= nvalid); s80-s82 added
# speedup vs baseline: 1.0097x; 1.0097x over previous
.LBB0_773:
	s_or_b64 exec, exec, s[12:13]
	v_and_b32_e32 v10, 32, v8
	v_bitop3_b32 v10, v2, v10, 48 bitop3:0x6c
	v_and_or_b32 v150, v0, 64, v10
	v_lshlrev_b32_e32 v0, 1, v9
	v_lshrrev_b32_e32 v2, 9, v2
	v_or_b32_e32 v138, v3, v150
	v_and_b32_e32 v0, 24, v0
	v_and_b32_e32 v2, 4, v2
	v_and_b32_e32 v3, 3, v9
	s_ashr_i32 s18, s20, 6
	v_or3_b32 v0, v2, v3, v0
	s_mov_b32 s12, 0x1fffe0
	s_lshl_b32 s29, s18, 10
	v_and_or_b32 v1, v1, s12, v0
	s_add_i32 s50, s29, 0
	v_lshl_or_b32 v128, v1, 11, v150
	s_add_i32 m0, s50, 0x10000
	s_ashr_i32 s21, s20, 8
	v_and_or_b32 v0, v5, s12, v0
	global_load_lds_dwordx4 v128, s[36:37]
	s_add_i32 m0, s50, 0x12000
	v_lshl_or_b32 v130, v0, 11, v150
	s_add_u32 s12, s36, 0x40000
	global_load_lds_dwordx4 v130, s[36:37]
	s_addc_u32 s13, s37, 0
	s_add_i32 m0, s50, 0x14000
	s_add_i32 s51, s50, 0x2000
	global_load_lds_dwordx4 v128, s[12:13]
	s_add_i32 m0, s50, 0x16000
	v_or_b32_e32 v136, v4, v150
	global_load_lds_dwordx4 v130, s[12:13]
	s_mov_b32 m0, s50
	s_add_i32 s52, s50, 0x4000
	global_load_lds_dwordx4 v138, s[30:31]
	s_mov_b32 m0, s51
	v_or_b32_e32 v134, v7, v150
	global_load_lds_dwordx4 v136, s[30:31]
	s_mov_b32 m0, s52
	s_add_i32 s53, s50, 0x6000
	v_or_b32_e32 v140, v6, v150
	global_load_lds_dwordx4 v134, s[30:31]
	s_mov_b32 m0, s53
	v_mov_b32_e32 v133, 0
	global_load_lds_dwordx4 v140, s[30:31]
	v_mov_b32_e32 v129, v133
	v_mov_b32_e32 v131, v133
	v_mov_b32_e32 v139, v133
	v_mov_b32_e32 v137, v133
	s_cmp_eq_u32 s21, 1
	s_mov_b32 s54, 0
	v_lshl_add_u64 v[6:7], s[36:37], 0, v[128:129]
	v_lshl_add_u64 v[4:5], s[36:37], 0, v[130:131]
	v_lshl_add_u64 v[0:1], s[30:31], 0, v[138:139]
	s_cselect_b64 s[12:13], -1, 0
	s_and_b32 s81, s12, 64
	s_add_i32 s82, s81, 0x80
	s_cmp_lg_u32 s21, 1
	v_lshl_add_u64 v[2:3], s[30:31], 0, v[136:137]
	s_cbranch_scc1 .LBB0_775
	s_barrier

.LBB0_791:
	ds_read_b128 v[160:163], v152
	ds_read_b128 v[164:167], v152 offset:1024
	ds_read_b128 v[168:171], v152 offset:2048
	ds_read_b128 v[172:175], v152 offset:3072
	ds_read_b128 v[176:179], v153
	ds_read_b128 v[180:183], v153 offset:1024
	ds_read_b128 v[184:187], v153 offset:2048
	ds_read_b128 v[188:191], v153 offset:3072
	s_add_u32 s38, s30, s36
	s_addc_u32 s39, s31, s37
	s_add_u32 s40, s38, 0x100
	s_addc_u32 s41, s39, 0
	s_add_u32 s68, s23, s36
	s_addc_u32 s69, s66, s37
	s_cmpk_eq_i32 s36, 0x700
	s_cselect_b64 vcc, -1, 0
	s_and_b64 s[38:39], vcc, exec
	v_cndmask_b32_e32 v132, v138, v157, vcc
	s_cselect_b32 s41, s27, s41
	s_cselect_b32 s40, s26, s40
	v_cndmask_b32_e32 v224, v136, v156, vcc
	v_cndmask_b32_e32 v135, v134, v155, vcc
	v_cndmask_b32_e32 v141, v140, v158, vcc
	s_cselect_b32 s39, s25, s69
	s_cselect_b32 s38, s24, s68
	s_mov_b32 m0, s60
	v_lshl_add_u64 v[226:227], v[144:145], 0, s[36:37]
	ds_read_b128 v[192:195], v154
	ds_read_b128 v[196:199], v154 offset:1024
	ds_read_b128 v[200:203], v154 offset:2048
	ds_read_b128 v[204:207], v154 offset:3072
	ds_read_b128 v[208:211], v154 offset:4096
	ds_read_b128 v[212:215], v154 offset:5120
	ds_read_b128 v[216:219], v154 offset:6144
	ds_read_b128 v[220:223], v154 offset:7168
	global_load_lds_dwordx4 v[226:227], off
	v_lshl_add_u64 v[226:227], v[142:143], 0, s[36:37]
	s_add_i32 m0, s50, 0xe000
	s_nop 0
	global_load_lds_dwordx4 v[226:227], off
	s_waitcnt vmcnt(8)
	s_waitcnt lgkmcnt(0)
	s_barrier
	s_cmp_le_i32 s80, s81
	s_cbranch_scc1 .Lmsk_64
	s_setprio 1
	s_waitcnt lgkmcnt(0)
	v_mfma_f32_16x16x32_bf16 v[116:119], v[160:163], v[192:195], v[116:119]
	v_mfma_f32_16x16x32_bf16 v[112:115], v[168:171], v[192:195], v[112:115]
	v_mfma_f32_16x16x32_bf16 v[108:111], v[160:163], v[200:203], v[108:111]
	v_mfma_f32_16x16x32_bf16 v[104:107], v[168:171], v[200:203], v[104:107]
	v_mfma_f32_16x16x32_bf16 v[92:95], v[160:163], v[208:211], v[92:95]
	v_mfma_f32_16x16x32_bf16 v[88:91], v[168:171], v[208:211], v[88:91]
	v_mfma_f32_16x16x32_bf16 v[76:79], v[160:163], v[216:219], v[76:79]
	v_mfma_f32_16x16x32_bf16 v[72:75], v[168:171], v[216:219], v[72:75]
	v_mfma_f32_16x16x32_bf16 v[116:119], v[164:167], v[196:199], v[116:119]
	v_mfma_f32_16x16x32_bf16 v[112:115], v[172:175], v[196:199], v[112:115]
	v_mfma_f32_16x16x32_bf16 v[108:111], v[164:167], v[204:207], v[108:111]
	v_mfma_f32_16x16x32_bf16 v[104:107], v[172:175], v[204:207], v[104:107]
	v_mfma_f32_16x16x32_bf16 v[92:95], v[164:167], v[212:215], v[92:95]
	v_mfma_f32_16x16x32_bf16 v[88:91], v[172:175], v[212:215], v[88:91]
	v_mfma_f32_16x16x32_bf16 v[76:79], v[164:167], v[220:223], v[76:79]
	v_mfma_f32_16x16x32_bf16 v[72:75], v[172:175], v[220:223], v[72:75]
	s_setprio 0
	s_setprio 1
	v_mfma_f32_16x16x32_bf16 v[124:127], v[176:179], v[192:195], v[124:127]
	v_mfma_f32_16x16x32_bf16 v[120:123], v[184:187], v[192:195], v[120:123]
	v_mfma_f32_16x16x32_bf16 v[100:103], v[176:179], v[200:203], v[100:103]
	v_mfma_f32_16x16x32_bf16 v[96:99], v[184:187], v[200:203], v[96:99]
	v_mfma_f32_16x16x32_bf16 v[84:87], v[176:179], v[208:211], v[84:87]
	v_mfma_f32_16x16x32_bf16 v[80:83], v[184:187], v[208:211], v[80:83]
	v_mfma_f32_16x16x32_bf16 v[68:71], v[176:179], v[216:219], v[68:71]
	v_mfma_f32_16x16x32_bf16 v[64:67], v[184:187], v[216:219], v[64:67]
	v_mfma_f32_16x16x32_bf16 v[124:127], v[180:183], v[196:199], v[124:127]
	v_mfma_f32_16x16x32_bf16 v[120:123], v[188:191], v[196:199], v[120:123]
	v_mfma_f32_16x16x32_bf16 v[100:103], v[180:183], v[204:207], v[100:103]
	v_mfma_f32_16x16x32_bf16 v[96:99], v[188:191], v[204:207], v[96:99]
	v_mfma_f32_16x16x32_bf16 v[84:87], v[180:183], v[212:215], v[84:87]
	v_mfma_f32_16x16x32_bf16 v[80:83], v[188:191], v[212:215], v[80:83]
	v_mfma_f32_16x16x32_bf16 v[68:71], v[180:183], v[220:223], v[68:71]
	v_mfma_f32_16x16x32_bf16 v[64:67], v[188:191], v[220:223], v[64:67]
	s_setprio 0
.Lmsk_64:
	s_barrier
	s_add_i32 s68, s57, s29
	v_lshl_add_u64 v[226:227], s[38:39], 0, v[128:129]
	s_mov_b32 m0, s68
	ds_read_b128 v[192:195], v154 offset:16384
	ds_read_b128 v[196:199], v154 offset:17408
	ds_read_b128 v[200:203], v154 offset:18432
	ds_read_b128 v[204:207], v154 offset:19456
	ds_read_b128 v[208:211], v154 offset:20480
	ds_read_b128 v[212:215], v154 offset:21504
	ds_read_b128 v[216:219], v154 offset:22528
	ds_read_b128 v[220:223], v154 offset:23552
	global_load_lds_dwordx4 v[226:227], off
	s_add_i32 m0, s68, 0x2000
	s_add_u32 s68, s38, 0x40000
	v_lshl_add_u64 v[228:229], s[38:39], 0, v[130:131]
	s_addc_u32 s69, s39, 0
	s_add_i32 s70, s58, s29
	global_load_lds_dwordx4 v[228:229], off
	v_lshl_add_u64 v[230:231], s[68:69], 0, v[128:129]
	s_mov_b32 m0, s70
	v_mov_b32_e32 v225, v133
	global_load_lds_dwordx4 v[230:231], off
	v_lshl_add_u64 v[230:231], s[68:69], 0, v[130:131]
	s_add_i32 m0, s70, 0x2000
	s_nop 0
	global_load_lds_dwordx4 v[230:231], off
	s_mov_b32 m0, s50
	v_lshl_add_u64 v[230:231], s[40:41], 0, v[132:133]
	global_load_lds_dwordx4 v132, s[40:41]
	s_mov_b32 m0, s51
	s_nop 0
	global_load_lds_dwordx4 v224, s[40:41]
	s_waitcnt vmcnt(8)
	s_waitcnt lgkmcnt(0)
	v_lshl_add_u64 v[224:225], s[40:41], 0, v[224:225]
	s_barrier
	s_cmp_le_i32 s80, s82
	s_cbranch_scc1 .Lmsk_63
	s_setprio 1
	s_waitcnt lgkmcnt(0)
	v_mfma_f32_16x16x32_bf16 v[60:63], v[160:163], v[192:195], v[60:63]
	v_mfma_f32_16x16x32_bf16 v[56:59], v[168:171], v[192:195], v[56:59]
	v_mfma_f32_16x16x32_bf16 v[44:47], v[160:163], v[200:203], v[44:47]
	v_mfma_f32_16x16x32_bf16 v[40:43], v[168:171], v[200:203], v[40:43]
	v_mfma_f32_16x16x32_bf16 v[28:31], v[160:163], v[208:211], v[28:31]
	v_mfma_f32_16x16x32_bf16 v[24:27], v[168:171], v[208:211], v[24:27]
	v_mfma_f32_16x16x32_bf16 v[12:15], v[160:163], v[216:219], v[12:15]
	v_mfma_f32_16x16x32_bf16 v[8:11], v[168:171], v[216:219], v[8:11]
	v_mfma_f32_16x16x32_bf16 v[60:63], v[164:167], v[196:199], v[60:63]
	v_mfma_f32_16x16x32_bf16 v[56:59], v[172:175], v[196:199], v[56:59]
	v_mfma_f32_16x16x32_bf16 v[44:47], v[164:167], v[204:207], v[44:47]
	v_mfma_f32_16x16x32_bf16 v[40:43], v[172:175], v[204:207], v[40:43]
	v_mfma_f32_16x16x32_bf16 v[28:31], v[164:167], v[212:215], v[28:31]
	v_mfma_f32_16x16x32_bf16 v[24:27], v[172:175], v[212:215], v[24:27]
	v_mfma_f32_16x16x32_bf16 v[12:15], v[164:167], v[220:223], v[12:15]
	v_mfma_f32_16x16x32_bf16 v[8:11], v[172:175], v[220:223], v[8:11]
	s_setprio 0
	s_setprio 1
	v_mfma_f32_16x16x32_bf16 v[52:55], v[176:179], v[192:195], v[52:55]
	v_mfma_f32_16x16x32_bf16 v[48:51], v[184:187], v[192:195], v[48:51]
	v_mfma_f32_16x16x32_bf16 v[36:39], v[176:179], v[200:203], v[36:39]
	v_mfma_f32_16x16x32_bf16 v[32:35], v[184:187], v[200:203], v[32:35]
	v_mfma_f32_16x16x32_bf16 v[20:23], v[176:179], v[208:211], v[20:23]
	v_mfma_f32_16x16x32_bf16 v[16:19], v[184:187], v[208:211], v[16:19]
	v_mfma_f32_16x16x32_bf16 v[4:7], v[176:179], v[216:219], v[4:7]
	v_mfma_f32_16x16x32_bf16 v[0:3], v[184:187], v[216:219], v[0:3]
	v_mfma_f32_16x16x32_bf16 v[52:55], v[180:183], v[196:199], v[52:55]
	v_mfma_f32_16x16x32_bf16 v[48:51], v[188:191], v[196:199], v[48:51]
	v_mfma_f32_16x16x32_bf16 v[36:39], v[180:183], v[204:207], v[36:39]
	v_mfma_f32_16x16x32_bf16 v[32:35], v[188:191], v[204:207], v[32:35]
	v_mfma_f32_16x16x32_bf16 v[20:23], v[180:183], v[212:215], v[20:23]
	v_mfma_f32_16x16x32_bf16 v[16:19], v[188:191], v[212:215], v[16:19]
	v_mfma_f32_16x16x32_bf16 v[4:7], v[180:183], v[220:223], v[4:7]
	v_mfma_f32_16x16x32_bf16 v[0:3], v[188:191], v[220:223], v[0:3]
	s_setprio 0
.Lmsk_63:
	s_barrier
	s_add_i32 s68, 0, 0x18000
	v_add_u32_e32 v132, s68, v139
	s_add_i32 s69, 0, 0x1c000
	ds_read_b128 v[160:163], v132
	ds_read_b128 v[164:167], v132 offset:1024
	ds_read_b128 v[168:171], v132 offset:2048
	ds_read_b128 v[172:175], v132 offset:3072
	v_add_u32_e32 v132, s69, v139
	ds_read_b128 v[176:179], v132
	ds_read_b128 v[180:183], v132 offset:1024
	ds_read_b128 v[184:187], v132 offset:2048
	ds_read_b128 v[188:191], v132 offset:3072
	s_mov_b32 m0, s52
	ds_read_b128 v[192:195], v154 offset:32768
	ds_read_b128 v[196:199], v154 offset:33792
	ds_read_b128 v[200:203], v154 offset:34816
	ds_read_b128 v[204:207], v154 offset:35840
	ds_read_b128 v[208:211], v154 offset:36864
	ds_read_b128 v[212:215], v154 offset:37888
	ds_read_b128 v[216:219], v154 offset:38912
	ds_read_b128 v[220:223], v154 offset:39936
	global_load_lds_dwordx4 v135, s[40:41]
	s_mov_b32 m0, s53
	s_nop 0
	global_load_lds_dwordx4 v141, s[40:41]
	s_waitcnt vmcnt(8)
	s_waitcnt lgkmcnt(0)
	s_barrier
	s_cmp_le_i32 s80, s81
	s_cbranch_scc1 .Lmsk_62
	s_setprio 1
	s_waitcnt lgkmcnt(0)
	v_mfma_f32_16x16x32_bf16 v[116:119], v[160:163], v[192:195], v[116:119]
	v_mfma_f32_16x16x32_bf16 v[112:115], v[168:171], v[192:195], v[112:115]
	v_mfma_f32_16x16x32_bf16 v[108:111], v[160:163], v[200:203], v[108:111]
	v_mfma_f32_16x16x32_bf16 v[104:107], v[168:171], v[200:203], v[104:107]
	v_mfma_f32_16x16x32_bf16 v[92:95], v[160:163], v[208:211], v[92:95]
	v_mfma_f32_16x16x32_bf16 v[88:91], v[168:171], v[208:211], v[88:91]
	v_mfma_f32_16x16x32_bf16 v[76:79], v[160:163], v[216:219], v[76:79]
	v_mfma_f32_16x16x32_bf16 v[72:75], v[168:171], v[216:219], v[72:75]
	v_mfma_f32_16x16x32_bf16 v[116:119], v[164:167], v[196:199], v[116:119]
	v_mfma_f32_16x16x32_bf16 v[112:115], v[172:175], v[196:199], v[112:115]
	v_mfma_f32_16x16x32_bf16 v[108:111], v[164:167], v[204:207], v[108:111]
	v_mfma_f32_16x16x32_bf16 v[104:107], v[172:175], v[204:207], v[104:107]
	v_mfma_f32_16x16x32_bf16 v[92:95], v[164:167], v[212:215], v[92:95]
	v_mfma_f32_16x16x32_bf16 v[88:91], v[172:175], v[212:215], v[88:91]
	v_mfma_f32_16x16x32_bf16 v[76:79], v[164:167], v[220:223], v[76:79]
	v_mfma_f32_16x16x32_bf16 v[72:75], v[172:175], v[220:223], v[72:75]
	s_setprio 0
	s_setprio 1
	v_mfma_f32_16x16x32_bf16 v[124:127], v[176:179], v[192:195], v[124:127]
	v_mfma_f32_16x16x32_bf16 v[120:123], v[184:187], v[192:195], v[120:123]
	v_mfma_f32_16x16x32_bf16 v[100:103], v[176:179], v[200:203], v[100:103]
	v_mfma_f32_16x16x32_bf16 v[96:99], v[184:187], v[200:203], v[96:99]
	v_mfma_f32_16x16x32_bf16 v[84:87], v[176:179], v[208:211], v[84:87]
	v_mfma_f32_16x16x32_bf16 v[80:83], v[184:187], v[208:211], v[80:83]
	v_mfma_f32_16x16x32_bf16 v[68:71], v[176:179], v[216:219], v[68:71]
	v_mfma_f32_16x16x32_bf16 v[64:67], v[184:187], v[216:219], v[64:67]
	v_mfma_f32_16x16x32_bf16 v[124:127], v[180:183], v[196:199], v[124:127]
	v_mfma_f32_16x16x32_bf16 v[120:123], v[188:191], v[196:199], v[120:123]
	v_mfma_f32_16x16x32_bf16 v[100:103], v[180:183], v[204:207], v[100:103]
	v_mfma_f32_16x16x32_bf16 v[96:99], v[188:191], v[204:207], v[96:99]
	v_mfma_f32_16x16x32_bf16 v[84:87], v[180:183], v[212:215], v[84:87]
	v_mfma_f32_16x16x32_bf16 v[80:83], v[188:191], v[212:215], v[80:83]
	v_mfma_f32_16x16x32_bf16 v[68:71], v[180:183], v[220:223], v[68:71]
	v_mfma_f32_16x16x32_bf16 v[64:67], v[188:191], v[220:223], v[64:67]
	s_setprio 0
.Lmsk_62:
	s_barrier
	s_add_i32 s40, s68, s29
	v_lshl_add_u64 v[226:227], v[226:227], 0, s[18:19]
	s_mov_b32 m0, s40
	ds_read_b128 v[192:195], v154 offset:49152
	ds_read_b128 v[196:199], v154 offset:50176
	ds_read_b128 v[200:203], v154 offset:51200
	ds_read_b128 v[204:207], v154 offset:52224
	ds_read_b128 v[208:211], v154 offset:53248
	ds_read_b128 v[212:215], v154 offset:54272
	ds_read_b128 v[216:219], v154 offset:55296
	ds_read_b128 v[220:223], v154 offset:56320
	global_load_lds_dwordx4 v[226:227], off
	s_add_i32 m0, s40, 0x2000
	s_add_u32 s38, s38, 0x40080
	v_lshl_add_u64 v[226:227], v[228:229], 0, s[18:19]
	s_addc_u32 s39, s39, 0
	s_add_i32 s40, s69, s29
	global_load_lds_dwordx4 v[226:227], off
	v_lshl_add_u64 v[226:227], s[38:39], 0, v[128:129]
	s_mov_b32 m0, s40
	v_lshl_add_u64 v[224:225], v[224:225], 0, s[18:19]
	global_load_lds_dwordx4 v[226:227], off
	v_lshl_add_u64 v[226:227], s[38:39], 0, v[130:131]
	s_add_i32 m0, s40, 0x2000
	s_nop 0
	global_load_lds_dwordx4 v[226:227], off
	v_lshl_add_u64 v[226:227], v[230:231], 0, s[18:19]
	s_mov_b32 m0, s55
	s_nop 0
	global_load_lds_dwordx4 v[226:227], off
	s_mov_b32 m0, s56
	s_nop 0
	global_load_lds_dwordx4 v[224:225], off
	s_waitcnt vmcnt(8)
	s_waitcnt lgkmcnt(0)
	s_barrier
	s_cmp_le_i32 s80, s82
	s_cbranch_scc1 .Lmsk_61
	s_setprio 1
	s_waitcnt lgkmcnt(0)
	v_mfma_f32_16x16x32_bf16 v[60:63], v[160:163], v[192:195], v[60:63]
	v_mfma_f32_16x16x32_bf16 v[56:59], v[168:171], v[192:195], v[56:59]
	v_mfma_f32_16x16x32_bf16 v[44:47], v[160:163], v[200:203], v[44:47]
	v_mfma_f32_16x16x32_bf16 v[40:43], v[168:171], v[200:203], v[40:43]
	v_mfma_f32_16x16x32_bf16 v[28:31], v[160:163], v[208:211], v[28:31]
	v_mfma_f32_16x16x32_bf16 v[24:27], v[168:171], v[208:211], v[24:27]
	v_mfma_f32_16x16x32_bf16 v[12:15], v[160:163], v[216:219], v[12:15]
	v_mfma_f32_16x16x32_bf16 v[8:11], v[168:171], v[216:219], v[8:11]
	v_mfma_f32_16x16x32_bf16 v[60:63], v[164:167], v[196:199], v[60:63]
	v_mfma_f32_16x16x32_bf16 v[56:59], v[172:175], v[196:199], v[56:59]
	v_mfma_f32_16x16x32_bf16 v[44:47], v[164:167], v[204:207], v[44:47]
	v_mfma_f32_16x16x32_bf16 v[40:43], v[172:175], v[204:207], v[40:43]
	v_mfma_f32_16x16x32_bf16 v[28:31], v[164:167], v[212:215], v[28:31]
	v_mfma_f32_16x16x32_bf16 v[24:27], v[172:175], v[212:215], v[24:27]
	v_mfma_f32_16x16x32_bf16 v[12:15], v[164:167], v[220:223], v[12:15]
	v_mfma_f32_16x16x32_bf16 v[8:11], v[172:175], v[220:223], v[8:11]
	s_setprio 0
	s_setprio 1
	v_mfma_f32_16x16x32_bf16 v[52:55], v[176:179], v[192:195], v[52:55]
	v_mfma_f32_16x16x32_bf16 v[48:51], v[184:187], v[192:195], v[48:51]
	v_mfma_f32_16x16x32_bf16 v[36:39], v[176:179], v[200:203], v[36:39]
	v_mfma_f32_16x16x32_bf16 v[32:35], v[184:187], v[200:203], v[32:35]
	v_mfma_f32_16x16x32_bf16 v[20:23], v[176:179], v[208:211], v[20:23]
	v_mfma_f32_16x16x32_bf16 v[16:19], v[184:187], v[208:211], v[16:19]
	v_mfma_f32_16x16x32_bf16 v[4:7], v[176:179], v[216:219], v[4:7]
	v_mfma_f32_16x16x32_bf16 v[0:3], v[184:187], v[216:219], v[0:3]
	v_mfma_f32_16x16x32_bf16 v[52:55], v[180:183], v[196:199], v[52:55]
	v_mfma_f32_16x16x32_bf16 v[48:51], v[188:191], v[196:199], v[48:51]
	v_mfma_f32_16x16x32_bf16 v[36:39], v[180:183], v[204:207], v[36:39]
	v_mfma_f32_16x16x32_bf16 v[32:35], v[188:191], v[204:207], v[32:35]
	v_mfma_f32_16x16x32_bf16 v[20:23], v[180:183], v[212:215], v[20:23]
	v_mfma_f32_16x16x32_bf16 v[16:19], v[188:191], v[212:215], v[16:19]
	v_mfma_f32_16x16x32_bf16 v[4:7], v[180:183], v[220:223], v[4:7]
	v_mfma_f32_16x16x32_bf16 v[0:3], v[188:191], v[220:223], v[0:3]
	s_setprio 0
.Lmsk_61:
	s_barrier
	s_add_i32 s67, s67, 2
	s_add_u32 s36, s36, 0x100
	s_addc_u32 s37, s37, 0
	s_cmp_gt_u32 s67, 13
	s_cbranch_scc0 .LBB0_791
	s_and_b64 vcc, exec, s[20:21]
	s_cbranch_vccz .LBB0_794
	s_barrier

.LBB0_1061:
	v_lshlrev_b32_e32 v1, 4, v0
	v_and_b32_e32 v2, 32, v8
	v_bitop3_b32 v2, v1, v2, 48 bitop3:0x6c
	v_lshrrev_b32_e32 v5, 1, v0
	v_lshrrev_b32_e32 v2, 1, v2
	v_bfe_u32 v3, v0, 2, 26
	v_bfe_u32 v4, v1, 6, 4
	v_and_or_b32 v2, v5, 32, v2
	v_and_b32_e32 v5, 48, v0
	v_lshrrev_b32_e32 v6, 5, v0
	v_lshrrev_b32_e32 v0, 3, v0
	s_mov_b32 s4, 0x1fffff0
	v_and_b32_e32 v6, 4, v6
	v_bfe_u32 v7, v1, 6, 2
	v_and_or_b32 v0, v0, s4, v4
	s_movk_i32 s6, 0x180
	v_or3_b32 v5, v7, v6, v5
	s_movk_i32 s5, 0xc0
	v_mul_lo_u32 v0, v0, s6
	v_and_or_b32 v3, v3, s5, v5
	v_or_b32_e32 v0, v0, v2
	v_lshlrev_b32_e32 v128, 1, v0
	v_mul_u32_u24_e32 v0, 0x180, v3
	v_or_b32_e32 v0, v0, v2
	s_ashr_i32 s14, s16, 6
	v_lshlrev_b32_e32 v130, 1, v0
	v_add_u32_e32 v0, 0x2000, v1
	v_lshrrev_b32_e32 v1, 7, v0
	v_lshrrev_b32_e32 v0, 6, v0
	s_lshl_b32 s46, s14, 10
	v_and_or_b32 v0, v0, s5, v5
	s_add_i32 s47, s46, 0
	v_mul_u32_u24_e32 v0, 0x180, v0
	s_add_i32 m0, s47, 0x10000
	v_or_b32_e32 v0, v0, v2
	s_ashr_i32 s17, s16, 8
	global_load_lds_dwordx4 v130, s[38:39]
	s_add_i32 m0, s47, 0x12000
	v_and_or_b32 v1, v1, s4, v4
	v_lshlrev_b32_e32 v134, 1, v0
	s_add_u32 s4, s38, 0x1800
	global_load_lds_dwordx4 v134, s[38:39]
	s_addc_u32 s5, s39, 0
	s_add_i32 m0, s47, 0x14000
	v_mul_lo_u32 v1, v1, s6
	global_load_lds_dwordx4 v130, s[4:5]
	s_add_i32 m0, s47, 0x16000
	s_add_i32 s48, s47, 0x2000
	v_or_b32_e32 v1, v1, v2
	global_load_lds_dwordx4 v134, s[4:5]
	s_mov_b32 m0, s47
	s_add_u32 s4, s36, 0x18000
	v_lshlrev_b32_e32 v132, 1, v1
	global_load_lds_dwordx4 v128, s[36:37]
	s_mov_b32 m0, s48
	s_addc_u32 s5, s37, 0
	s_add_i32 s50, s47, 0x4000
	global_load_lds_dwordx4 v132, s[36:37]
	s_mov_b32 m0, s50
	s_add_i32 s51, s47, 0x6000
	global_load_lds_dwordx4 v128, s[4:5]
	s_mov_b32 m0, s51
	v_mov_b32_e32 v131, 0
	global_load_lds_dwordx4 v132, s[4:5]
	v_mov_b32_e32 v135, v131
	v_mov_b32_e32 v129, v131
	v_mov_b32_e32 v133, v131
	s_cmp_eq_u32 s17, 1
	v_lshl_add_u64 v[6:7], s[38:39], 0, v[130:131]
	v_lshl_add_u64 v[4:5], s[38:39], 0, v[134:135]
	v_lshl_add_u64 v[0:1], s[36:37], 0, v[128:129]
	s_cselect_b64 s[4:5], -1, 0
	s_and_b32 s81, s4, 64
	s_add_i32 s82, s81, 0x80
	s_cmp_lg_u32 s17, 1
	v_lshl_add_u64 v[2:3], s[36:37], 0, v[132:133]
	s_cbranch_scc1 .LBB0_1063
	s_barrier

.LBB0_1068:
	ds_read_b128 v[8:11], v149
	ds_read_b128 v[12:15], v149 offset:1024
	ds_read_b128 v[16:19], v149 offset:2048
	ds_read_b128 v[20:23], v149 offset:3072
	ds_read_b128 v[24:27], v150
	ds_read_b128 v[28:31], v150 offset:1024
	ds_read_b128 v[32:35], v150 offset:2048
	ds_read_b128 v[36:39], v150 offset:3072
	s_add_u32 s68, s36, 0x18080
	s_addc_u32 s69, s37, 0
	s_mov_b32 m0, s62
	v_lshl_add_u64 v[64:65], s[68:69], 0, v[128:129]
	ds_read_b128 v[0:3], v140
	ds_read_b128 v[4:7], v140 offset:1024
	ds_read_b128 v[40:43], v140 offset:2048
	ds_read_b128 v[44:47], v140 offset:3072
	ds_read_b128 v[48:51], v140 offset:4096
	ds_read_b128 v[52:55], v140 offset:5120
	ds_read_b128 v[56:59], v140 offset:6144
	ds_read_b128 v[60:63], v140 offset:7168
	global_load_lds_dwordx4 v[64:65], off
	v_lshl_add_u64 v[64:65], s[68:69], 0, v[132:133]
	s_mov_b32 m0, s63
	s_nop 0
	global_load_lds_dwordx4 v[64:65], off
	s_waitcnt vmcnt(8)
	s_waitcnt lgkmcnt(0)
	s_barrier
	s_cmp_le_i32 s52, s81
	s_cbranch_scc1 .Lmsk_60
	s_setprio 1
	s_waitcnt lgkmcnt(0)
	v_mfma_f32_16x16x32_bf16 v[64:67], v[8:11], v[0:3], 0
	v_mfma_f32_16x16x32_bf16 v[68:71], v[16:19], v[0:3], 0
	v_mfma_f32_16x16x32_bf16 v[72:75], v[8:11], v[40:43], 0
	v_mfma_f32_16x16x32_bf16 v[76:79], v[16:19], v[40:43], 0
	v_mfma_f32_16x16x32_bf16 v[80:83], v[8:11], v[48:51], 0
	v_mfma_f32_16x16x32_bf16 v[84:87], v[16:19], v[48:51], 0
	v_mfma_f32_16x16x32_bf16 v[88:91], v[8:11], v[56:59], 0
	v_mfma_f32_16x16x32_bf16 v[92:95], v[16:19], v[56:59], 0
	v_mfma_f32_16x16x32_bf16 v[64:67], v[12:15], v[4:7], v[64:67]
	v_mfma_f32_16x16x32_bf16 v[68:71], v[20:23], v[4:7], v[68:71]
	v_mfma_f32_16x16x32_bf16 v[72:75], v[12:15], v[44:47], v[72:75]
	v_mfma_f32_16x16x32_bf16 v[76:79], v[20:23], v[44:47], v[76:79]
	v_mfma_f32_16x16x32_bf16 v[80:83], v[12:15], v[52:55], v[80:83]
	v_mfma_f32_16x16x32_bf16 v[84:87], v[20:23], v[52:55], v[84:87]
	v_mfma_f32_16x16x32_bf16 v[88:91], v[12:15], v[60:63], v[88:91]
	v_mfma_f32_16x16x32_bf16 v[92:95], v[20:23], v[60:63], v[92:95]
	s_setprio 0
	s_setprio 1
	v_mfma_f32_16x16x32_bf16 v[96:99], v[24:27], v[0:3], 0
	v_mfma_f32_16x16x32_bf16 v[0:3], v[32:35], v[0:3], 0
	v_mfma_f32_16x16x32_bf16 v[100:103], v[36:39], v[4:7], v[0:3]
	v_mfma_f32_16x16x32_bf16 v[0:3], v[24:27], v[40:43], 0
	v_mfma_f32_16x16x32_bf16 v[104:107], v[28:31], v[44:47], v[0:3]
	v_mfma_f32_16x16x32_bf16 v[0:3], v[32:35], v[40:43], 0
	v_mfma_f32_16x16x32_bf16 v[40:43], v[36:39], v[44:47], v[0:3]
	v_mfma_f32_16x16x32_bf16 v[0:3], v[24:27], v[48:51], 0
	v_mfma_f32_16x16x32_bf16 v[44:47], v[28:31], v[52:55], v[0:3]
	v_mfma_f32_16x16x32_bf16 v[0:3], v[32:35], v[48:51], 0
	v_mfma_f32_16x16x32_bf16 v[48:51], v[36:39], v[52:55], v[0:3]
	v_mfma_f32_16x16x32_bf16 v[0:3], v[24:27], v[56:59], 0
	v_mfma_f32_16x16x32_bf16 v[52:55], v[28:31], v[60:63], v[0:3]
	v_mfma_f32_16x16x32_bf16 v[0:3], v[32:35], v[56:59], 0
	v_mfma_f32_16x16x32_bf16 v[96:99], v[28:31], v[4:7], v[96:99]
	v_mfma_f32_16x16x32_bf16 v[56:59], v[36:39], v[60:63], v[0:3]
	s_setprio 0
.Lmsk_60:
	s_barrier
	s_nop 3
	v_lshl_add_u64 v[0:1], s[38:39], 0, v[130:131]
	s_add_i32 s71, s60, s46
	v_lshl_add_u64 v[2:3], v[0:1], 0, s[18:19]
	s_mov_b32 m0, s71
	s_add_i32 s68, s71, 0x2000
	ds_read_b128 v[60:63], v140 offset:16384
	ds_read_b128 v[108:111], v140 offset:17408
	ds_read_b128 v[112:115], v140 offset:18432
	ds_read_b128 v[116:119], v140 offset:19456
	ds_read_b128 v[120:123], v140 offset:20480
	ds_read_b128 v[124:127], v140 offset:21504
	ds_read_b128 v[152:155], v140 offset:22528
	ds_read_b128 v[156:159], v140 offset:23552
	global_load_lds_dwordx4 v[2:3], off
	v_lshl_add_u64 v[2:3], s[38:39], 0, v[134:135]
	s_add_u32 s72, s38, 0x1900
	v_lshl_add_u64 v[4:5], v[2:3], 0, s[18:19]
	s_mov_b32 m0, s68
	s_addc_u32 s73, s39, 0
	s_add_i32 s69, s61, s46
	global_load_lds_dwordx4 v[4:5], off
	v_lshl_add_u64 v[4:5], s[72:73], 0, v[130:131]
	s_mov_b32 m0, s69
	s_add_i32 s70, s69, 0x2000
	global_load_lds_dwordx4 v[4:5], off
	v_lshl_add_u64 v[4:5], s[72:73], 0, v[134:135]
	s_mov_b32 m0, s70
	s_nop 0
	global_load_lds_dwordx4 v[4:5], off
	v_lshl_add_u64 v[4:5], s[36:37], 0, v[128:129]
	v_lshl_add_u64 v[6:7], v[4:5], 0, s[18:19]
	s_mov_b32 m0, s47
	s_nop 0
	global_load_lds_dwordx4 v[6:7], off
	v_lshl_add_u64 v[6:7], s[36:37], 0, v[132:133]
	v_lshl_add_u64 v[136:137], v[6:7], 0, s[18:19]
	s_mov_b32 m0, s48
	s_nop 0
	global_load_lds_dwordx4 v[136:137], off
	s_waitcnt vmcnt(8)
	s_waitcnt lgkmcnt(0)
	s_barrier
	s_cmp_le_i32 s52, s82
	s_cbranch_scc1 .Lmsk_59
	s_setprio 1
	s_waitcnt lgkmcnt(0)
	v_mfma_f32_16x16x32_bf16 v[160:163], v[8:11], v[60:63], 0
	v_mfma_f32_16x16x32_bf16 v[168:171], v[8:11], v[112:115], 0
	v_mfma_f32_16x16x32_bf16 v[176:179], v[8:11], v[120:123], 0
	v_mfma_f32_16x16x32_bf16 v[8:11], v[8:11], v[152:155], 0
	v_mfma_f32_16x16x32_bf16 v[160:163], v[12:15], v[108:111], v[160:163]
	v_mfma_f32_16x16x32_bf16 v[164:167], v[16:19], v[60:63], 0
	v_mfma_f32_16x16x32_bf16 v[168:171], v[12:15], v[116:119], v[168:171]
	v_mfma_f32_16x16x32_bf16 v[172:175], v[16:19], v[112:115], 0
	v_mfma_f32_16x16x32_bf16 v[176:179], v[12:15], v[124:127], v[176:179]
	v_mfma_f32_16x16x32_bf16 v[180:183], v[16:19], v[120:123], 0
	v_mfma_f32_16x16x32_bf16 v[10:13], v[12:15], v[156:159], v[8:11]
	v_mfma_f32_16x16x32_bf16 v[14:17], v[16:19], v[152:155], 0
	v_mfma_f32_16x16x32_bf16 v[14:17], v[20:23], v[156:159], v[14:17]
	v_mfma_f32_16x16x32_bf16 v[164:167], v[20:23], v[108:111], v[164:167]
	v_mfma_f32_16x16x32_bf16 v[172:175], v[20:23], v[116:119], v[172:175]
	v_mfma_f32_16x16x32_bf16 v[180:183], v[20:23], v[124:127], v[180:183]
	s_setprio 0
	s_setprio 1
	v_mfma_f32_16x16x32_bf16 v[18:21], v[24:27], v[60:63], 0
	v_mfma_f32_16x16x32_bf16 v[60:63], v[32:35], v[60:63], 0
	v_mfma_f32_16x16x32_bf16 v[18:21], v[28:31], v[108:111], v[18:21]
	v_mfma_f32_16x16x32_bf16 v[60:63], v[36:39], v[108:111], v[60:63]
	v_mfma_f32_16x16x32_bf16 v[108:111], v[24:27], v[112:115], 0
	v_mfma_f32_16x16x32_bf16 v[112:115], v[32:35], v[112:115], 0
	v_mfma_f32_16x16x32_bf16 v[108:111], v[28:31], v[116:119], v[108:111]
	v_mfma_f32_16x16x32_bf16 v[112:115], v[36:39], v[116:119], v[112:115]
	v_mfma_f32_16x16x32_bf16 v[116:119], v[24:27], v[120:123], 0
	v_mfma_f32_16x16x32_bf16 v[22:25], v[24:27], v[152:155], 0
	v_mfma_f32_16x16x32_bf16 v[116:119], v[28:31], v[124:127], v[116:119]
	v_mfma_f32_16x16x32_bf16 v[120:123], v[32:35], v[120:123], 0
	v_mfma_f32_16x16x32_bf16 v[22:25], v[28:31], v[156:159], v[22:25]
	v_mfma_f32_16x16x32_bf16 v[26:29], v[32:35], v[152:155], 0
	v_mfma_f32_16x16x32_bf16 v[120:123], v[36:39], v[124:127], v[120:123]
	v_mfma_f32_16x16x32_bf16 v[26:29], v[36:39], v[156:159], v[26:29]
	s_setprio 0
.Lmsk_59:
	s_barrier
	s_add_i32 s75, 0, 0x18000
	s_add_i32 s74, 0, 0x1c000
	v_add_u32_e32 v8, s75, v139
	v_add_u32_e32 v9, s74, v139
	ds_read_b128 v[30:33], v8
	ds_read_b128 v[34:37], v8 offset:1024
	ds_read_b128 v[124:127], v8 offset:2048
	ds_read_b128 v[152:155], v8 offset:3072
	ds_read_b128 v[156:159], v9
	ds_read_b128 v[184:187], v9 offset:1024
	ds_read_b128 v[188:191], v9 offset:2048
	ds_read_b128 v[192:195], v9 offset:3072
	s_add_u32 s72, s36, 0x18100
	s_addc_u32 s73, s37, 0
	s_mov_b32 m0, s50
	v_lshl_add_u64 v[38:39], s[72:73], 0, v[128:129]
	ds_read_b128 v[196:199], v140 offset:32768
	ds_read_b128 v[200:203], v140 offset:33792
	ds_read_b128 v[204:207], v140 offset:34816
	ds_read_b128 v[208:211], v140 offset:35840
	ds_read_b128 v[212:215], v140 offset:36864
	ds_read_b128 v[216:219], v140 offset:37888
	ds_read_b128 v[220:223], v140 offset:38912
	ds_read_b128 v[224:227], v140 offset:39936
	global_load_lds_dwordx4 v[38:39], off
	v_lshl_add_u64 v[38:39], s[72:73], 0, v[132:133]
	s_mov_b32 m0, s51
	s_nop 0
	global_load_lds_dwordx4 v[38:39], off
	s_waitcnt vmcnt(8)
	s_waitcnt lgkmcnt(0)
	s_barrier
	s_cmp_le_i32 s52, s81
	s_cbranch_scc1 .Lmsk_58
	s_setprio 1
	s_waitcnt lgkmcnt(0)
	v_mfma_f32_16x16x32_bf16 v[64:67], v[30:33], v[196:199], v[64:67]
	v_mfma_f32_16x16x32_bf16 v[68:71], v[124:127], v[196:199], v[68:71]
	v_mfma_f32_16x16x32_bf16 v[72:75], v[30:33], v[204:207], v[72:75]
	v_mfma_f32_16x16x32_bf16 v[76:79], v[124:127], v[204:207], v[76:79]
	v_mfma_f32_16x16x32_bf16 v[80:83], v[30:33], v[212:215], v[80:83]
	v_mfma_f32_16x16x32_bf16 v[84:87], v[124:127], v[212:215], v[84:87]
	v_mfma_f32_16x16x32_bf16 v[88:91], v[30:33], v[220:223], v[88:91]
	v_mfma_f32_16x16x32_bf16 v[92:95], v[124:127], v[220:223], v[92:95]
	v_mfma_f32_16x16x32_bf16 v[64:67], v[34:37], v[200:203], v[64:67]
	v_mfma_f32_16x16x32_bf16 v[68:71], v[152:155], v[200:203], v[68:71]
	v_mfma_f32_16x16x32_bf16 v[72:75], v[34:37], v[208:211], v[72:75]
	v_mfma_f32_16x16x32_bf16 v[76:79], v[152:155], v[208:211], v[76:79]
	v_mfma_f32_16x16x32_bf16 v[80:83], v[34:37], v[216:219], v[80:83]
	v_mfma_f32_16x16x32_bf16 v[84:87], v[152:155], v[216:219], v[84:87]
	v_mfma_f32_16x16x32_bf16 v[88:91], v[34:37], v[224:227], v[88:91]
	v_mfma_f32_16x16x32_bf16 v[92:95], v[152:155], v[224:227], v[92:95]
	s_setprio 0
	s_setprio 1
	v_mfma_f32_16x16x32_bf16 v[96:99], v[156:159], v[196:199], v[96:99]
	v_mfma_f32_16x16x32_bf16 v[100:103], v[188:191], v[196:199], v[100:103]
	v_mfma_f32_16x16x32_bf16 v[104:107], v[156:159], v[204:207], v[104:107]
	v_mfma_f32_16x16x32_bf16 v[38:41], v[188:191], v[204:207], v[40:43]
	v_mfma_f32_16x16x32_bf16 v[42:45], v[156:159], v[212:215], v[44:47]
	v_mfma_f32_16x16x32_bf16 v[46:49], v[188:191], v[212:215], v[48:51]
	v_mfma_f32_16x16x32_bf16 v[50:53], v[156:159], v[220:223], v[52:55]
	v_mfma_f32_16x16x32_bf16 v[54:57], v[188:191], v[220:223], v[56:59]
	v_mfma_f32_16x16x32_bf16 v[96:99], v[184:187], v[200:203], v[96:99]
	v_mfma_f32_16x16x32_bf16 v[100:103], v[192:195], v[200:203], v[100:103]
	v_mfma_f32_16x16x32_bf16 v[104:107], v[184:187], v[208:211], v[104:107]
	v_mfma_f32_16x16x32_bf16 v[38:41], v[192:195], v[208:211], v[38:41]
	v_mfma_f32_16x16x32_bf16 v[42:45], v[184:187], v[216:219], v[42:45]
	v_mfma_f32_16x16x32_bf16 v[46:49], v[192:195], v[216:219], v[46:49]
	v_mfma_f32_16x16x32_bf16 v[50:53], v[184:187], v[224:227], v[50:53]
	v_mfma_f32_16x16x32_bf16 v[54:57], v[192:195], v[224:227], v[54:57]
	s_setprio 0
.Lmsk_58:
	s_barrier
	s_add_i32 s75, s75, s46
	s_add_i32 s72, s75, 0x2000
	v_lshl_add_u64 v[58:59], v[0:1], 0, s[20:21]
	s_mov_b32 m0, s75
	s_add_u32 s76, s38, 0x1980
	ds_read_b128 v[196:199], v140 offset:49152
	ds_read_b128 v[200:203], v140 offset:50176
	ds_read_b128 v[204:207], v140 offset:51200
	ds_read_b128 v[208:211], v140 offset:52224
	ds_read_b128 v[212:215], v140 offset:53248
	ds_read_b128 v[216:219], v140 offset:54272
	ds_read_b128 v[220:223], v140 offset:55296
	ds_read_b128 v[224:227], v140 offset:56320
	global_load_lds_dwordx4 v[58:59], off
	v_lshl_add_u64 v[58:59], v[2:3], 0, s[20:21]
	s_mov_b32 m0, s72
	s_addc_u32 s77, s39, 0
	s_add_i32 s73, s74, s46
	global_load_lds_dwordx4 v[58:59], off
	v_lshl_add_u64 v[58:59], s[76:77], 0, v[130:131]
	s_mov_b32 m0, s73
	s_add_i32 s74, s73, 0x2000
	global_load_lds_dwordx4 v[58:59], off
	v_lshl_add_u64 v[58:59], s[76:77], 0, v[134:135]
	s_mov_b32 m0, s74
	s_nop 0
	global_load_lds_dwordx4 v[58:59], off
	v_lshl_add_u64 v[58:59], v[4:5], 0, s[20:21]
	s_mov_b32 m0, s53
	s_nop 0
	global_load_lds_dwordx4 v[58:59], off
	v_lshl_add_u64 v[58:59], v[6:7], 0, s[20:21]
	s_mov_b32 m0, s54
	s_nop 0
	global_load_lds_dwordx4 v[58:59], off
	s_waitcnt vmcnt(8)
	s_waitcnt lgkmcnt(0)
	s_barrier
	s_cmp_le_i32 s52, s82
	s_cbranch_scc1 .Lmsk_57
	s_setprio 1
	s_waitcnt lgkmcnt(0)
	v_mfma_f32_16x16x32_bf16 v[10:13], v[30:33], v[220:223], v[10:13]
	v_mfma_f32_16x16x32_bf16 v[14:17], v[124:127], v[220:223], v[14:17]
	v_mfma_f32_16x16x32_bf16 v[160:163], v[30:33], v[196:199], v[160:163]
	v_mfma_f32_16x16x32_bf16 v[164:167], v[124:127], v[196:199], v[164:167]
	v_mfma_f32_16x16x32_bf16 v[168:171], v[30:33], v[204:207], v[168:171]
	v_mfma_f32_16x16x32_bf16 v[172:175], v[124:127], v[204:207], v[172:175]
	v_mfma_f32_16x16x32_bf16 v[176:179], v[30:33], v[212:215], v[176:179]
	v_mfma_f32_16x16x32_bf16 v[180:183], v[124:127], v[212:215], v[180:183]
	v_mfma_f32_16x16x32_bf16 v[10:13], v[34:37], v[224:227], v[10:13]
	v_mfma_f32_16x16x32_bf16 v[14:17], v[152:155], v[224:227], v[14:17]
	v_mfma_f32_16x16x32_bf16 v[160:163], v[34:37], v[200:203], v[160:163]
	v_mfma_f32_16x16x32_bf16 v[164:167], v[152:155], v[200:203], v[164:167]
	v_mfma_f32_16x16x32_bf16 v[168:171], v[34:37], v[208:211], v[168:171]
	v_mfma_f32_16x16x32_bf16 v[172:175], v[152:155], v[208:211], v[172:175]
	v_mfma_f32_16x16x32_bf16 v[176:179], v[34:37], v[216:219], v[176:179]
	v_mfma_f32_16x16x32_bf16 v[180:183], v[152:155], v[216:219], v[180:183]
	s_setprio 0
	s_setprio 1
	v_mfma_f32_16x16x32_bf16 v[18:21], v[156:159], v[196:199], v[18:21]
	v_mfma_f32_16x16x32_bf16 v[30:33], v[188:191], v[196:199], v[60:63]
	v_mfma_f32_16x16x32_bf16 v[34:37], v[156:159], v[204:207], v[108:111]
	v_mfma_f32_16x16x32_bf16 v[58:61], v[188:191], v[204:207], v[112:115]
	v_mfma_f32_16x16x32_bf16 v[108:111], v[156:159], v[212:215], v[116:119]
	v_mfma_f32_16x16x32_bf16 v[112:115], v[188:191], v[212:215], v[120:123]
	v_mfma_f32_16x16x32_bf16 v[22:25], v[156:159], v[220:223], v[22:25]
	v_mfma_f32_16x16x32_bf16 v[26:29], v[188:191], v[220:223], v[26:29]
	v_mfma_f32_16x16x32_bf16 v[18:21], v[184:187], v[200:203], v[18:21]
	v_mfma_f32_16x16x32_bf16 v[30:33], v[192:195], v[200:203], v[30:33]
	v_mfma_f32_16x16x32_bf16 v[34:37], v[184:187], v[208:211], v[34:37]
	v_mfma_f32_16x16x32_bf16 v[58:61], v[192:195], v[208:211], v[58:61]
	v_mfma_f32_16x16x32_bf16 v[108:111], v[184:187], v[216:219], v[108:111]
	v_mfma_f32_16x16x32_bf16 v[112:115], v[192:195], v[216:219], v[112:115]
	v_mfma_f32_16x16x32_bf16 v[22:25], v[184:187], v[224:227], v[22:25]
	v_mfma_f32_16x16x32_bf16 v[26:29], v[192:195], v[224:227], v[26:29]
	s_setprio 0
.Lmsk_57:
	s_barrier
	ds_read_b128 v[116:119], v149
	ds_read_b128 v[120:123], v149 offset:1024
	ds_read_b128 v[124:127], v149 offset:2048
	ds_read_b128 v[152:155], v149 offset:3072
	ds_read_b128 v[156:159], v150
	ds_read_b128 v[184:187], v150 offset:1024
	ds_read_b128 v[188:191], v150 offset:2048
	ds_read_b128 v[192:195], v150 offset:3072
	s_add_u32 s76, s36, 0x18180
	s_addc_u32 s77, s37, 0
	s_mov_b32 m0, s62
	v_lshl_add_u64 v[62:63], s[76:77], 0, v[128:129]
	ds_read_b128 v[196:199], v140
	ds_read_b128 v[200:203], v140 offset:1024
	ds_read_b128 v[204:207], v140 offset:2048
	ds_read_b128 v[208:211], v140 offset:3072
	ds_read_b128 v[212:215], v140 offset:4096
	ds_read_b128 v[216:219], v140 offset:5120
	ds_read_b128 v[220:223], v140 offset:6144
	ds_read_b128 v[224:227], v140 offset:7168
	global_load_lds_dwordx4 v[62:63], off
	v_lshl_add_u64 v[62:63], s[76:77], 0, v[132:133]
	s_mov_b32 m0, s63
	s_nop 0
	global_load_lds_dwordx4 v[62:63], off
	s_waitcnt vmcnt(8)
	s_waitcnt lgkmcnt(0)
	s_barrier
	s_cmp_le_i32 s52, s81
	s_cbranch_scc1 .Lmsk_56
	s_setprio 1
	s_waitcnt lgkmcnt(0)
	v_mfma_f32_16x16x32_bf16 v[62:65], v[116:119], v[196:199], v[64:67]
	v_mfma_f32_16x16x32_bf16 v[66:69], v[124:127], v[196:199], v[68:71]
	v_mfma_f32_16x16x32_bf16 v[70:73], v[116:119], v[204:207], v[72:75]
	v_mfma_f32_16x16x32_bf16 v[74:77], v[124:127], v[204:207], v[76:79]
	v_mfma_f32_16x16x32_bf16 v[78:81], v[116:119], v[212:215], v[80:83]
	v_mfma_f32_16x16x32_bf16 v[82:85], v[124:127], v[212:215], v[84:87]
	v_mfma_f32_16x16x32_bf16 v[86:89], v[116:119], v[220:223], v[88:91]
	v_mfma_f32_16x16x32_bf16 v[90:93], v[124:127], v[220:223], v[92:95]
	v_mfma_f32_16x16x32_bf16 v[62:65], v[120:123], v[200:203], v[62:65]
	v_mfma_f32_16x16x32_bf16 v[66:69], v[152:155], v[200:203], v[66:69]
	v_mfma_f32_16x16x32_bf16 v[70:73], v[120:123], v[208:211], v[70:73]
	v_mfma_f32_16x16x32_bf16 v[74:77], v[152:155], v[208:211], v[74:77]
	v_mfma_f32_16x16x32_bf16 v[78:81], v[120:123], v[216:219], v[78:81]
	v_mfma_f32_16x16x32_bf16 v[82:85], v[152:155], v[216:219], v[82:85]
	v_mfma_f32_16x16x32_bf16 v[86:89], v[120:123], v[224:227], v[86:89]
	v_mfma_f32_16x16x32_bf16 v[90:93], v[152:155], v[224:227], v[90:93]
	s_setprio 0
	s_setprio 1
	v_mfma_f32_16x16x32_bf16 v[94:97], v[156:159], v[196:199], v[96:99]
	v_mfma_f32_16x16x32_bf16 v[98:101], v[188:191], v[196:199], v[100:103]
	v_mfma_f32_16x16x32_bf16 v[102:105], v[156:159], v[204:207], v[104:107]
	v_mfma_f32_16x16x32_bf16 v[38:41], v[188:191], v[204:207], v[38:41]
	v_mfma_f32_16x16x32_bf16 v[42:45], v[156:159], v[212:215], v[42:45]
	v_mfma_f32_16x16x32_bf16 v[46:49], v[188:191], v[212:215], v[46:49]
	v_mfma_f32_16x16x32_bf16 v[50:53], v[156:159], v[220:223], v[50:53]
	v_mfma_f32_16x16x32_bf16 v[54:57], v[188:191], v[220:223], v[54:57]
	v_mfma_f32_16x16x32_bf16 v[94:97], v[184:187], v[200:203], v[94:97]
	v_mfma_f32_16x16x32_bf16 v[98:101], v[192:195], v[200:203], v[98:101]
	v_mfma_f32_16x16x32_bf16 v[102:105], v[184:187], v[208:211], v[102:105]
	v_mfma_f32_16x16x32_bf16 v[38:41], v[192:195], v[208:211], v[38:41]
	v_mfma_f32_16x16x32_bf16 v[42:45], v[184:187], v[216:219], v[42:45]
	v_mfma_f32_16x16x32_bf16 v[46:49], v[192:195], v[216:219], v[46:49]
	v_mfma_f32_16x16x32_bf16 v[50:53], v[184:187], v[224:227], v[50:53]
	v_mfma_f32_16x16x32_bf16 v[54:57], v[192:195], v[224:227], v[54:57]
	s_setprio 0
.Lmsk_56:
	s_barrier
	s_mov_b32 m0, s71
	v_lshl_add_u64 v[106:107], v[0:1], 0, s[22:23]
	s_add_u32 s76, s38, 0x1a00
	ds_read_b128 v[196:199], v140 offset:16384
	ds_read_b128 v[200:203], v140 offset:17408
	ds_read_b128 v[204:207], v140 offset:18432
	ds_read_b128 v[208:211], v140 offset:19456
	ds_read_b128 v[212:215], v140 offset:20480
	ds_read_b128 v[216:219], v140 offset:21504
	ds_read_b128 v[220:223], v140 offset:22528
	ds_read_b128 v[224:227], v140 offset:23552
	global_load_lds_dwordx4 v[106:107], off
	v_lshl_add_u64 v[106:107], v[2:3], 0, s[22:23]
	s_mov_b32 m0, s68
	s_addc_u32 s77, s39, 0
	global_load_lds_dwordx4 v[106:107], off
	v_lshl_add_u64 v[106:107], s[76:77], 0, v[130:131]
	s_mov_b32 m0, s69
	s_nop 0
	global_load_lds_dwordx4 v[106:107], off
	v_lshl_add_u64 v[106:107], s[76:77], 0, v[134:135]
	s_mov_b32 m0, s70
	s_nop 0
	global_load_lds_dwordx4 v[106:107], off
	v_lshl_add_u64 v[106:107], v[4:5], 0, s[22:23]
	s_mov_b32 m0, s47
	s_nop 0
	global_load_lds_dwordx4 v[106:107], off
	v_lshl_add_u64 v[106:107], v[6:7], 0, s[22:23]
	s_mov_b32 m0, s48
	s_nop 0
	global_load_lds_dwordx4 v[106:107], off
	s_waitcnt vmcnt(8)
	s_waitcnt lgkmcnt(0)
	s_barrier
	s_cmp_le_i32 s52, s82
	s_cbranch_scc1 .Lmsk_55
	s_setprio 1
	s_waitcnt lgkmcnt(0)
	v_mfma_f32_16x16x32_bf16 v[10:13], v[116:119], v[220:223], v[10:13]
	v_mfma_f32_16x16x32_bf16 v[14:17], v[124:127], v[220:223], v[14:17]
	v_mfma_f32_16x16x32_bf16 v[160:163], v[116:119], v[196:199], v[160:163]
	v_mfma_f32_16x16x32_bf16 v[164:167], v[124:127], v[196:199], v[164:167]
	v_mfma_f32_16x16x32_bf16 v[168:171], v[116:119], v[204:207], v[168:171]
	v_mfma_f32_16x16x32_bf16 v[172:175], v[124:127], v[204:207], v[172:175]
	v_mfma_f32_16x16x32_bf16 v[176:179], v[116:119], v[212:215], v[176:179]
	v_mfma_f32_16x16x32_bf16 v[180:183], v[124:127], v[212:215], v[180:183]
	v_mfma_f32_16x16x32_bf16 v[10:13], v[120:123], v[224:227], v[10:13]
	v_mfma_f32_16x16x32_bf16 v[14:17], v[152:155], v[224:227], v[14:17]
	v_mfma_f32_16x16x32_bf16 v[160:163], v[120:123], v[200:203], v[160:163]
	v_mfma_f32_16x16x32_bf16 v[164:167], v[152:155], v[200:203], v[164:167]
	v_mfma_f32_16x16x32_bf16 v[168:171], v[120:123], v[208:211], v[168:171]
	v_mfma_f32_16x16x32_bf16 v[172:175], v[152:155], v[208:211], v[172:175]
	v_mfma_f32_16x16x32_bf16 v[176:179], v[120:123], v[216:219], v[176:179]
	v_mfma_f32_16x16x32_bf16 v[180:183], v[152:155], v[216:219], v[180:183]
	s_setprio 0
	s_setprio 1
	v_mfma_f32_16x16x32_bf16 v[18:21], v[156:159], v[196:199], v[18:21]
	v_mfma_f32_16x16x32_bf16 v[30:33], v[188:191], v[196:199], v[30:33]
	v_mfma_f32_16x16x32_bf16 v[34:37], v[156:159], v[204:207], v[34:37]
	v_mfma_f32_16x16x32_bf16 v[58:61], v[188:191], v[204:207], v[58:61]
	v_mfma_f32_16x16x32_bf16 v[106:109], v[156:159], v[212:215], v[108:111]
	v_mfma_f32_16x16x32_bf16 v[110:113], v[188:191], v[212:215], v[112:115]
	v_mfma_f32_16x16x32_bf16 v[22:25], v[156:159], v[220:223], v[22:25]
	v_mfma_f32_16x16x32_bf16 v[26:29], v[188:191], v[220:223], v[26:29]
	v_mfma_f32_16x16x32_bf16 v[18:21], v[184:187], v[200:203], v[18:21]
	v_mfma_f32_16x16x32_bf16 v[30:33], v[192:195], v[200:203], v[30:33]
	v_mfma_f32_16x16x32_bf16 v[34:37], v[184:187], v[208:211], v[34:37]
	v_mfma_f32_16x16x32_bf16 v[58:61], v[192:195], v[208:211], v[58:61]
	v_mfma_f32_16x16x32_bf16 v[106:109], v[184:187], v[216:219], v[106:109]
	v_mfma_f32_16x16x32_bf16 v[110:113], v[192:195], v[216:219], v[110:113]
	v_mfma_f32_16x16x32_bf16 v[22:25], v[184:187], v[224:227], v[22:25]
	v_mfma_f32_16x16x32_bf16 v[26:29], v[192:195], v[224:227], v[26:29]
	s_setprio 0
.Lmsk_55:
	s_barrier
	ds_read_b128 v[114:117], v8
	ds_read_b128 v[118:121], v8 offset:1024
	ds_read_b128 v[122:125], v8 offset:2048
	ds_read_b128 v[152:155], v8 offset:3072
	ds_read_b128 v[156:159], v9
	ds_read_b128 v[184:187], v9 offset:1024
	ds_read_b128 v[188:191], v9 offset:2048
	ds_read_b128 v[192:195], v9 offset:3072
	s_add_u32 s76, s36, 0x18200
	s_addc_u32 s77, s37, 0
	s_mov_b32 m0, s50
	v_lshl_add_u64 v[126:127], s[76:77], 0, v[128:129]
	ds_read_b128 v[196:199], v140 offset:32768
	ds_read_b128 v[200:203], v140 offset:33792
	ds_read_b128 v[204:207], v140 offset:34816
	ds_read_b128 v[208:211], v140 offset:35840
	ds_read_b128 v[212:215], v140 offset:36864
	ds_read_b128 v[216:219], v140 offset:37888
	ds_read_b128 v[220:223], v140 offset:38912
	ds_read_b128 v[224:227], v140 offset:39936
	global_load_lds_dwordx4 v[126:127], off
	v_lshl_add_u64 v[126:127], s[76:77], 0, v[132:133]
	s_mov_b32 m0, s51
	s_nop 0
	global_load_lds_dwordx4 v[126:127], off
	s_waitcnt vmcnt(8)
	s_waitcnt lgkmcnt(0)
	s_barrier
	s_cmp_le_i32 s52, s81
	s_cbranch_scc1 .Lmsk_54
	s_setprio 1
	s_waitcnt lgkmcnt(0)
	v_mfma_f32_16x16x32_bf16 v[62:65], v[114:117], v[196:199], v[62:65]
	v_mfma_f32_16x16x32_bf16 v[66:69], v[122:125], v[196:199], v[66:69]
	v_mfma_f32_16x16x32_bf16 v[70:73], v[114:117], v[204:207], v[70:73]
	v_mfma_f32_16x16x32_bf16 v[74:77], v[122:125], v[204:207], v[74:77]
	v_mfma_f32_16x16x32_bf16 v[78:81], v[114:117], v[212:215], v[78:81]
	v_mfma_f32_16x16x32_bf16 v[82:85], v[122:125], v[212:215], v[82:85]
	v_mfma_f32_16x16x32_bf16 v[86:89], v[114:117], v[220:223], v[86:89]
	v_mfma_f32_16x16x32_bf16 v[90:93], v[122:125], v[220:223], v[90:93]
	v_mfma_f32_16x16x32_bf16 v[62:65], v[118:121], v[200:203], v[62:65]
	v_mfma_f32_16x16x32_bf16 v[66:69], v[152:155], v[200:203], v[66:69]
	v_mfma_f32_16x16x32_bf16 v[70:73], v[118:121], v[208:211], v[70:73]
	v_mfma_f32_16x16x32_bf16 v[74:77], v[152:155], v[208:211], v[74:77]
	v_mfma_f32_16x16x32_bf16 v[78:81], v[118:121], v[216:219], v[78:81]
	v_mfma_f32_16x16x32_bf16 v[82:85], v[152:155], v[216:219], v[82:85]
	v_mfma_f32_16x16x32_bf16 v[86:89], v[118:121], v[224:227], v[86:89]
	v_mfma_f32_16x16x32_bf16 v[90:93], v[152:155], v[224:227], v[90:93]
	s_setprio 0
	s_setprio 1
	v_mfma_f32_16x16x32_bf16 v[94:97], v[156:159], v[196:199], v[94:97]
	v_mfma_f32_16x16x32_bf16 v[98:101], v[188:191], v[196:199], v[98:101]
	v_mfma_f32_16x16x32_bf16 v[102:105], v[156:159], v[204:207], v[102:105]
	v_mfma_f32_16x16x32_bf16 v[38:41], v[188:191], v[204:207], v[38:41]
	v_mfma_f32_16x16x32_bf16 v[42:45], v[156:159], v[212:215], v[42:45]
	v_mfma_f32_16x16x32_bf16 v[46:49], v[188:191], v[212:215], v[46:49]
	v_mfma_f32_16x16x32_bf16 v[50:53], v[156:159], v[220:223], v[50:53]
	v_mfma_f32_16x16x32_bf16 v[54:57], v[188:191], v[220:223], v[54:57]
	v_mfma_f32_16x16x32_bf16 v[94:97], v[184:187], v[200:203], v[94:97]
	v_mfma_f32_16x16x32_bf16 v[98:101], v[192:195], v[200:203], v[98:101]
	v_mfma_f32_16x16x32_bf16 v[102:105], v[184:187], v[208:211], v[102:105]
	v_mfma_f32_16x16x32_bf16 v[38:41], v[192:195], v[208:211], v[38:41]
	v_mfma_f32_16x16x32_bf16 v[42:45], v[184:187], v[216:219], v[42:45]
	v_mfma_f32_16x16x32_bf16 v[46:49], v[192:195], v[216:219], v[46:49]
	v_mfma_f32_16x16x32_bf16 v[50:53], v[184:187], v[224:227], v[50:53]
	v_mfma_f32_16x16x32_bf16 v[54:57], v[192:195], v[224:227], v[54:57]
	s_setprio 0
.Lmsk_54:
	s_barrier
	s_mov_b32 m0, s75
	v_lshl_add_u64 v[0:1], v[0:1], 0, s[24:25]
	s_add_u32 s38, s38, 0x1a80
	ds_read_b128 v[196:199], v140 offset:49152
	ds_read_b128 v[200:203], v140 offset:50176
	ds_read_b128 v[204:207], v140 offset:51200
	ds_read_b128 v[208:211], v140 offset:52224
	ds_read_b128 v[212:215], v140 offset:53248
	ds_read_b128 v[216:219], v140 offset:54272
	ds_read_b128 v[220:223], v140 offset:55296
	ds_read_b128 v[224:227], v140 offset:56320
	global_load_lds_dwordx4 v[0:1], off
	v_lshl_add_u64 v[0:1], v[2:3], 0, s[24:25]
	s_mov_b32 m0, s72
	s_addc_u32 s39, s39, 0
	global_load_lds_dwordx4 v[0:1], off
	v_lshl_add_u64 v[0:1], s[38:39], 0, v[130:131]
	s_mov_b32 m0, s73
	s_nop 0
	global_load_lds_dwordx4 v[0:1], off
	v_lshl_add_u64 v[0:1], s[38:39], 0, v[134:135]
	s_mov_b32 m0, s74
	s_nop 0
	global_load_lds_dwordx4 v[0:1], off
	v_lshl_add_u64 v[0:1], v[4:5], 0, s[24:25]
	s_mov_b32 m0, s53
	s_nop 0
	global_load_lds_dwordx4 v[0:1], off
	v_lshl_add_u64 v[0:1], v[6:7], 0, s[24:25]
	s_mov_b32 m0, s54
	s_nop 0
	global_load_lds_dwordx4 v[0:1], off
	s_waitcnt vmcnt(8)
	s_waitcnt lgkmcnt(0)
	s_barrier
	s_cmp_le_i32 s52, s82
	s_cbranch_scc1 .Lmsk_53
	s_setprio 1
	s_waitcnt lgkmcnt(0)
	v_mfma_f32_16x16x32_bf16 v[0:3], v[114:117], v[196:199], v[160:163]
	v_mfma_f32_16x16x32_bf16 v[4:7], v[122:125], v[196:199], v[164:167]
	v_mfma_f32_16x16x32_bf16 v[10:13], v[114:117], v[220:223], v[10:13]
	v_mfma_f32_16x16x32_bf16 v[14:17], v[122:125], v[220:223], v[14:17]
	v_mfma_f32_16x16x32_bf16 v[0:3], v[118:121], v[200:203], v[0:3]
	v_mfma_f32_16x16x32_bf16 v[4:7], v[152:155], v[200:203], v[4:7]
	v_mfma_f32_16x16x32_bf16 v[160:163], v[114:117], v[204:207], v[168:171]
	v_mfma_f32_16x16x32_bf16 v[164:167], v[122:125], v[204:207], v[172:175]
	v_mfma_f32_16x16x32_bf16 v[168:171], v[114:117], v[212:215], v[176:179]
	v_mfma_f32_16x16x32_bf16 v[172:175], v[122:125], v[212:215], v[180:183]
	v_mfma_f32_16x16x32_bf16 v[10:13], v[118:121], v[224:227], v[10:13]
	v_mfma_f32_16x16x32_bf16 v[14:17], v[152:155], v[224:227], v[14:17]
	v_mfma_f32_16x16x32_bf16 v[160:163], v[118:121], v[208:211], v[160:163]
	v_mfma_f32_16x16x32_bf16 v[164:167], v[152:155], v[208:211], v[164:167]
	v_mfma_f32_16x16x32_bf16 v[168:171], v[118:121], v[216:219], v[168:171]
	v_mfma_f32_16x16x32_bf16 v[172:175], v[152:155], v[216:219], v[172:175]
	s_setprio 0
	s_setprio 1
	v_mfma_f32_16x16x32_bf16 v[18:21], v[156:159], v[196:199], v[18:21]
	v_mfma_f32_16x16x32_bf16 v[30:33], v[188:191], v[196:199], v[30:33]
	v_mfma_f32_16x16x32_bf16 v[34:37], v[156:159], v[204:207], v[34:37]
	v_mfma_f32_16x16x32_bf16 v[58:61], v[188:191], v[204:207], v[58:61]
	v_mfma_f32_16x16x32_bf16 v[106:109], v[156:159], v[212:215], v[106:109]
	v_mfma_f32_16x16x32_bf16 v[110:113], v[188:191], v[212:215], v[110:113]
	v_mfma_f32_16x16x32_bf16 v[22:25], v[156:159], v[220:223], v[22:25]
	v_mfma_f32_16x16x32_bf16 v[26:29], v[188:191], v[220:223], v[26:29]
	v_mfma_f32_16x16x32_bf16 v[18:21], v[184:187], v[200:203], v[18:21]
	v_mfma_f32_16x16x32_bf16 v[30:33], v[192:195], v[200:203], v[30:33]
	v_mfma_f32_16x16x32_bf16 v[34:37], v[184:187], v[208:211], v[34:37]
	v_mfma_f32_16x16x32_bf16 v[58:61], v[192:195], v[208:211], v[58:61]
	v_mfma_f32_16x16x32_bf16 v[106:109], v[184:187], v[216:219], v[106:109]
	v_mfma_f32_16x16x32_bf16 v[110:113], v[192:195], v[216:219], v[110:113]
	v_mfma_f32_16x16x32_bf16 v[22:25], v[184:187], v[224:227], v[22:25]
	v_mfma_f32_16x16x32_bf16 v[26:29], v[192:195], v[224:227], v[26:29]
	s_setprio 0
.Lmsk_53:
	s_barrier
	ds_read_b128 v[114:117], v149
	ds_read_b128 v[118:121], v149 offset:1024
	ds_read_b128 v[122:125], v149 offset:2048
	ds_read_b128 v[152:155], v149 offset:3072
	ds_read_b128 v[156:159], v150
	ds_read_b128 v[176:179], v150 offset:1024
	ds_read_b128 v[180:183], v150 offset:2048
	ds_read_b128 v[184:187], v150 offset:3072
	s_add_u32 s36, s36, 0x18280
	s_addc_u32 s37, s37, 0
	s_mov_b32 m0, s62
	v_lshl_add_u64 v[126:127], s[36:37], 0, v[128:129]
	ds_read_b128 v[188:191], v140
	ds_read_b128 v[192:195], v140 offset:1024
	ds_read_b128 v[196:199], v140 offset:2048
	ds_read_b128 v[200:203], v140 offset:3072
	ds_read_b128 v[204:207], v140 offset:4096
	ds_read_b128 v[208:211], v140 offset:5120
	ds_read_b128 v[212:215], v140 offset:6144
	ds_read_b128 v[216:219], v140 offset:7168
	global_load_lds_dwordx4 v[126:127], off
	v_lshl_add_u64 v[126:127], s[36:37], 0, v[132:133]
	s_mov_b32 m0, s63
	s_nop 0
	global_load_lds_dwordx4 v[126:127], off
	s_waitcnt vmcnt(8)
	s_waitcnt lgkmcnt(0)
	s_barrier
	s_cmp_le_i32 s52, s81
	s_cbranch_scc1 .Lmsk_52
	s_setprio 1
	s_waitcnt lgkmcnt(0)
	v_mfma_f32_16x16x32_bf16 v[82:85], v[122:125], v[204:207], v[82:85]
	v_mfma_f32_16x16x32_bf16 v[220:223], v[152:155], v[208:211], v[82:85]
	v_mfma_f32_16x16x32_bf16 v[82:85], v[114:117], v[212:215], v[86:89]
	v_mfma_f32_16x16x32_bf16 v[62:65], v[114:117], v[188:191], v[62:65]
	v_mfma_f32_16x16x32_bf16 v[66:69], v[122:125], v[188:191], v[66:69]
	v_mfma_f32_16x16x32_bf16 v[70:73], v[114:117], v[196:199], v[70:73]
	v_mfma_f32_16x16x32_bf16 v[74:77], v[122:125], v[196:199], v[74:77]
	v_mfma_f32_16x16x32_bf16 v[78:81], v[114:117], v[204:207], v[78:81]
	v_mfma_f32_16x16x32_bf16 v[224:227], v[118:121], v[216:219], v[82:85]
	v_mfma_f32_16x16x32_bf16 v[82:85], v[122:125], v[212:215], v[90:93]
	v_mfma_f32_16x16x32_bf16 v[62:65], v[118:121], v[192:195], v[62:65]
	v_mfma_f32_16x16x32_bf16 v[66:69], v[152:155], v[192:195], v[66:69]
	v_mfma_f32_16x16x32_bf16 v[70:73], v[118:121], v[200:203], v[70:73]
	v_mfma_f32_16x16x32_bf16 v[74:77], v[152:155], v[200:203], v[74:77]
	v_mfma_f32_16x16x32_bf16 v[78:81], v[118:121], v[208:211], v[78:81]
	v_mfma_f32_16x16x32_bf16 v[88:91], v[152:155], v[216:219], v[82:85]
	s_setprio 0
	s_setprio 1
	v_mfma_f32_16x16x32_bf16 v[82:85], v[156:159], v[188:191], v[94:97]
	v_mfma_f32_16x16x32_bf16 v[92:95], v[176:179], v[192:195], v[82:85]
	v_mfma_f32_16x16x32_bf16 v[82:85], v[180:183], v[188:191], v[98:101]
	v_mfma_f32_16x16x32_bf16 v[38:41], v[180:183], v[196:199], v[38:41]
	v_mfma_f32_16x16x32_bf16 v[42:45], v[156:159], v[204:207], v[42:45]
	v_mfma_f32_16x16x32_bf16 v[46:49], v[180:183], v[204:207], v[46:49]
	v_mfma_f32_16x16x32_bf16 v[50:53], v[156:159], v[212:215], v[50:53]
	v_mfma_f32_16x16x32_bf16 v[54:57], v[180:183], v[212:215], v[54:57]
	v_mfma_f32_16x16x32_bf16 v[188:191], v[184:187], v[192:195], v[82:85]
	v_mfma_f32_16x16x32_bf16 v[82:85], v[156:159], v[196:199], v[102:105]
	v_mfma_f32_16x16x32_bf16 v[38:41], v[184:187], v[200:203], v[38:41]
	v_mfma_f32_16x16x32_bf16 v[42:45], v[176:179], v[208:211], v[42:45]
	v_mfma_f32_16x16x32_bf16 v[46:49], v[184:187], v[208:211], v[46:49]
	v_mfma_f32_16x16x32_bf16 v[50:53], v[176:179], v[216:219], v[50:53]
	v_mfma_f32_16x16x32_bf16 v[54:57], v[184:187], v[216:219], v[54:57]
	v_mfma_f32_16x16x32_bf16 v[192:195], v[176:179], v[200:203], v[82:85]
	s_setprio 0
.Lmsk_52:
	s_barrier
	s_mov_b32 m0, s71
	v_lshl_add_u64 v[136:137], s[28:29], 0, v[130:131]
	s_add_u32 s36, s28, 0x1800
	ds_read_b128 v[82:85], v140 offset:16384
	ds_read_b128 v[96:99], v140 offset:17408
	ds_read_b128 v[100:103], v140 offset:18432
	ds_read_b128 v[196:199], v140 offset:19456
	ds_read_b128 v[200:203], v140 offset:20480
	ds_read_b128 v[204:207], v140 offset:21504
	ds_read_b128 v[208:211], v140 offset:22528
	ds_read_b128 v[212:215], v140 offset:23552
	global_load_lds_dwordx4 v[136:137], off
	v_lshl_add_u64 v[142:143], s[28:29], 0, v[134:135]
	s_mov_b32 m0, s68
	s_addc_u32 s37, s29, 0
	global_load_lds_dwordx4 v[142:143], off
	v_lshl_add_u64 v[86:87], s[36:37], 0, v[130:131]
	s_mov_b32 m0, s69
	v_lshl_add_u64 v[144:145], s[26:27], 0, v[128:129]
	global_load_lds_dwordx4 v[86:87], off
	v_lshl_add_u64 v[86:87], s[36:37], 0, v[134:135]
	s_mov_b32 m0, s70
	v_lshl_add_u64 v[146:147], s[26:27], 0, v[132:133]
	global_load_lds_dwordx4 v[86:87], off
	s_mov_b32 m0, s47
	s_nop 0
	global_load_lds_dwordx4 v[144:145], off
	s_mov_b32 m0, s48
	s_nop 0
	global_load_lds_dwordx4 v[146:147], off
	s_waitcnt vmcnt(8)
	s_waitcnt lgkmcnt(0)
	s_barrier
	s_cmp_le_i32 s52, s82
	s_cbranch_scc1 .Lmsk_51
	s_setprio 1
	s_waitcnt lgkmcnt(0)
	v_mfma_f32_16x16x32_bf16 v[0:3], v[114:117], v[82:85], v[0:3]
	v_mfma_f32_16x16x32_bf16 v[4:7], v[122:125], v[82:85], v[4:7]
	v_mfma_f32_16x16x32_bf16 v[10:13], v[114:117], v[208:211], v[10:13]
	v_mfma_f32_16x16x32_bf16 v[0:3], v[118:121], v[96:99], v[0:3]
	v_mfma_f32_16x16x32_bf16 v[4:7], v[152:155], v[96:99], v[4:7]
	v_mfma_f32_16x16x32_bf16 v[160:163], v[114:117], v[100:103], v[160:163]
	v_mfma_f32_16x16x32_bf16 v[164:167], v[122:125], v[100:103], v[164:167]
	v_mfma_f32_16x16x32_bf16 v[168:171], v[114:117], v[200:203], v[168:171]
	v_mfma_f32_16x16x32_bf16 v[172:175], v[122:125], v[200:203], v[172:175]
	v_mfma_f32_16x16x32_bf16 v[10:13], v[118:121], v[212:215], v[10:13]
	v_mfma_f32_16x16x32_bf16 v[14:17], v[122:125], v[208:211], v[14:17]
	v_mfma_f32_16x16x32_bf16 v[160:163], v[118:121], v[196:199], v[160:163]
	v_mfma_f32_16x16x32_bf16 v[164:167], v[152:155], v[196:199], v[164:167]
	v_mfma_f32_16x16x32_bf16 v[168:171], v[118:121], v[204:207], v[168:171]
	v_mfma_f32_16x16x32_bf16 v[172:175], v[152:155], v[204:207], v[172:175]
	v_mfma_f32_16x16x32_bf16 v[152:155], v[152:155], v[212:215], v[14:17]
	s_setprio 0
	s_setprio 1
	v_mfma_f32_16x16x32_bf16 v[14:17], v[156:159], v[82:85], v[18:21]
	v_mfma_f32_16x16x32_bf16 v[216:219], v[176:179], v[96:99], v[14:17]
	v_mfma_f32_16x16x32_bf16 v[14:17], v[180:183], v[82:85], v[30:33]
	v_mfma_f32_16x16x32_bf16 v[228:231], v[184:187], v[96:99], v[14:17]
	v_mfma_f32_16x16x32_bf16 v[14:17], v[156:159], v[100:103], v[34:37]
	v_mfma_f32_16x16x32_bf16 v[232:235], v[176:179], v[196:199], v[14:17]
	v_mfma_f32_16x16x32_bf16 v[14:17], v[180:183], v[100:103], v[58:61]
	v_mfma_f32_16x16x32_bf16 v[196:199], v[184:187], v[196:199], v[14:17]
	v_mfma_f32_16x16x32_bf16 v[14:17], v[156:159], v[200:203], v[106:109]
	v_mfma_f32_16x16x32_bf16 v[236:239], v[176:179], v[204:207], v[14:17]
	v_mfma_f32_16x16x32_bf16 v[14:17], v[180:183], v[200:203], v[110:113]
	v_mfma_f32_16x16x32_bf16 v[200:203], v[184:187], v[204:207], v[14:17]
	v_mfma_f32_16x16x32_bf16 v[14:17], v[156:159], v[208:211], v[22:25]
	v_mfma_f32_16x16x32_bf16 v[156:159], v[176:179], v[212:215], v[14:17]
	v_mfma_f32_16x16x32_bf16 v[14:17], v[180:183], v[208:211], v[26:29]
	v_mfma_f32_16x16x32_bf16 v[176:179], v[184:187], v[212:215], v[14:17]
	s_setprio 0
.Lmsk_51:
	s_barrier
	ds_read_b128 v[24:27], v8
	ds_read_b128 v[28:31], v8 offset:1024
	ds_read_b128 v[58:61], v8 offset:2048
	ds_read_b128 v[180:183], v8 offset:3072
	ds_read_b128 v[184:187], v9
	ds_read_b128 v[204:207], v9 offset:1024
	ds_read_b128 v[208:211], v9 offset:2048
	ds_read_b128 v[212:215], v9 offset:3072
	s_add_u32 s36, s26, 0x18000
	s_addc_u32 s37, s27, 0
	s_mov_b32 m0, s50
	v_lshl_add_u64 v[8:9], s[36:37], 0, v[128:129]
	ds_read_b128 v[14:17], v140 offset:32768
	ds_read_b128 v[18:21], v140 offset:33792
	ds_read_b128 v[32:35], v140 offset:34816
	ds_read_b128 v[108:111], v140 offset:35840
	ds_read_b128 v[240:243], v140 offset:36864
	ds_read_b128 v[244:247], v140 offset:37888
	ds_read_b128 v[248:251], v140 offset:38912
	ds_read_b128 v[252:255], v140 offset:39936
	global_load_lds_dwordx4 v[8:9], off
	v_lshl_add_u64 v[8:9], s[36:37], 0, v[132:133]
	s_mov_b32 m0, s51
	s_nop 0
	global_load_lds_dwordx4 v[8:9], off
	s_waitcnt vmcnt(8)
	s_waitcnt lgkmcnt(0)
	s_barrier
	s_cmp_le_i32 s52, s81
	s_cbranch_scc1 .Lmsk_50
	s_setprio 1
	s_waitcnt lgkmcnt(0)
	v_mfma_f32_16x16x32_bf16 v[62:65], v[24:27], v[14:17], v[62:65]
	v_mfma_f32_16x16x32_bf16 v[112:115], v[28:31], v[18:21], v[62:65]
	v_mfma_f32_16x16x32_bf16 v[62:65], v[58:61], v[14:17], v[66:69]
	v_mfma_f32_16x16x32_bf16 v[116:119], v[180:183], v[18:21], v[62:65]
	v_mfma_f32_16x16x32_bf16 v[62:65], v[24:27], v[32:35], v[70:73]
	v_mfma_f32_16x16x32_bf16 v[96:99], v[28:31], v[108:111], v[62:65]
	v_mfma_f32_16x16x32_bf16 v[62:65], v[58:61], v[32:35], v[74:77]
	v_mfma_f32_16x16x32_bf16 v[100:103], v[180:183], v[108:111], v[62:65]
	v_mfma_f32_16x16x32_bf16 v[62:65], v[24:27], v[240:243], v[78:81]
	v_mfma_f32_16x16x32_bf16 v[80:83], v[28:31], v[244:247], v[62:65]
	v_mfma_f32_16x16x32_bf16 v[62:65], v[58:61], v[240:243], v[220:223]
	v_mfma_f32_16x16x32_bf16 v[84:87], v[180:183], v[244:247], v[62:65]
	v_mfma_f32_16x16x32_bf16 v[62:65], v[24:27], v[248:251], v[224:227]
	v_mfma_f32_16x16x32_bf16 v[68:71], v[58:61], v[248:251], v[88:91]
	v_mfma_f32_16x16x32_bf16 v[64:67], v[28:31], v[252:255], v[62:65]
	v_mfma_f32_16x16x32_bf16 v[68:71], v[180:183], v[252:255], v[68:71]
	s_setprio 0
	s_setprio 1
	v_mfma_f32_16x16x32_bf16 v[72:75], v[184:187], v[14:17], v[92:95]
	v_mfma_f32_16x16x32_bf16 v[14:17], v[208:211], v[14:17], v[188:191]
	v_mfma_f32_16x16x32_bf16 v[124:127], v[212:215], v[18:21], v[14:17]
	v_mfma_f32_16x16x32_bf16 v[14:17], v[184:187], v[32:35], v[192:195]
	v_mfma_f32_16x16x32_bf16 v[104:107], v[204:207], v[108:111], v[14:17]
	v_mfma_f32_16x16x32_bf16 v[14:17], v[208:211], v[32:35], v[38:41]
	v_mfma_f32_16x16x32_bf16 v[108:111], v[212:215], v[108:111], v[14:17]
	v_mfma_f32_16x16x32_bf16 v[14:17], v[184:187], v[240:243], v[42:45]
	v_mfma_f32_16x16x32_bf16 v[88:91], v[204:207], v[244:247], v[14:17]
	v_mfma_f32_16x16x32_bf16 v[14:17], v[208:211], v[240:243], v[46:49]
	v_mfma_f32_16x16x32_bf16 v[92:95], v[212:215], v[244:247], v[14:17]
	v_mfma_f32_16x16x32_bf16 v[14:17], v[184:187], v[248:251], v[50:53]
	v_mfma_f32_16x16x32_bf16 v[120:123], v[204:207], v[18:21], v[72:75]
	v_mfma_f32_16x16x32_bf16 v[72:75], v[204:207], v[252:255], v[14:17]
	v_mfma_f32_16x16x32_bf16 v[14:17], v[208:211], v[248:251], v[54:57]
	v_mfma_f32_16x16x32_bf16 v[76:79], v[212:215], v[252:255], v[14:17]
	s_setprio 0
.Lmsk_50:
	s_barrier
	s_mov_b32 m0, s75
	v_lshl_add_u64 v[8:9], v[136:137], 0, s[14:15]
	s_add_u32 s36, s28, 0x1880
	ds_read_b128 v[40:43], v140 offset:49152
	ds_read_b128 v[44:47], v140 offset:50176
	ds_read_b128 v[188:191], v140 offset:51200
	ds_read_b128 v[192:195], v140 offset:52224
	ds_read_b128 v[220:223], v140 offset:53248
	ds_read_b128 v[224:227], v140 offset:54272
	ds_read_b128 v[240:243], v140 offset:55296
	ds_read_b128 v[244:247], v140 offset:56320
	global_load_lds_dwordx4 v[8:9], off
	v_lshl_add_u64 v[8:9], v[142:143], 0, s[14:15]
	s_mov_b32 m0, s72
	s_addc_u32 s37, s29, 0
	global_load_lds_dwordx4 v[8:9], off
	v_lshl_add_u64 v[8:9], s[36:37], 0, v[130:131]
	s_mov_b32 m0, s73
	s_nop 0
	global_load_lds_dwordx4 v[8:9], off
	v_lshl_add_u64 v[8:9], s[36:37], 0, v[134:135]
	s_mov_b32 m0, s74
	s_nop 0
	global_load_lds_dwordx4 v[8:9], off
	v_lshl_add_u64 v[8:9], v[144:145], 0, s[14:15]
	s_mov_b32 m0, s53
	s_nop 0
	global_load_lds_dwordx4 v[8:9], off
	v_lshl_add_u64 v[8:9], v[146:147], 0, s[14:15]
	s_mov_b32 m0, s54
	s_nop 0
	global_load_lds_dwordx4 v[8:9], off
	s_waitcnt vmcnt(8)
	s_waitcnt lgkmcnt(0)
	s_barrier
	s_cmp_le_i32 s52, s82
	s_cbranch_scc1 .Lmsk_49
	s_setprio 1
	s_waitcnt lgkmcnt(0)
	v_mfma_f32_16x16x32_bf16 v[0:3], v[24:27], v[40:43], v[0:3]
	v_mfma_f32_16x16x32_bf16 v[48:51], v[28:31], v[44:47], v[0:3]
	v_mfma_f32_16x16x32_bf16 v[0:3], v[58:61], v[40:43], v[4:7]
	v_mfma_f32_16x16x32_bf16 v[52:55], v[180:183], v[44:47], v[0:3]
	v_mfma_f32_16x16x32_bf16 v[0:3], v[24:27], v[188:191], v[160:163]
	v_mfma_f32_16x16x32_bf16 v[32:35], v[28:31], v[192:195], v[0:3]
	v_mfma_f32_16x16x32_bf16 v[0:3], v[58:61], v[188:191], v[164:167]
	v_mfma_f32_16x16x32_bf16 v[36:39], v[180:183], v[192:195], v[0:3]
	v_mfma_f32_16x16x32_bf16 v[0:3], v[24:27], v[220:223], v[168:171]
	v_mfma_f32_16x16x32_bf16 v[16:19], v[28:31], v[224:227], v[0:3]
	v_mfma_f32_16x16x32_bf16 v[0:3], v[58:61], v[220:223], v[172:175]
	v_mfma_f32_16x16x32_bf16 v[20:23], v[180:183], v[224:227], v[0:3]
	v_mfma_f32_16x16x32_bf16 v[0:3], v[24:27], v[240:243], v[10:13]
	v_mfma_f32_16x16x32_bf16 v[4:7], v[58:61], v[240:243], v[152:155]
	v_mfma_f32_16x16x32_bf16 v[0:3], v[28:31], v[244:247], v[0:3]
	v_mfma_f32_16x16x32_bf16 v[4:7], v[180:183], v[244:247], v[4:7]
	s_setprio 0
	s_setprio 1
	v_mfma_f32_16x16x32_bf16 v[8:11], v[184:187], v[40:43], v[216:219]
	v_mfma_f32_16x16x32_bf16 v[56:59], v[204:207], v[44:47], v[8:11]
	v_mfma_f32_16x16x32_bf16 v[8:11], v[208:211], v[40:43], v[228:231]
	v_mfma_f32_16x16x32_bf16 v[60:63], v[212:215], v[44:47], v[8:11]
	v_mfma_f32_16x16x32_bf16 v[8:11], v[184:187], v[188:191], v[232:235]
	v_mfma_f32_16x16x32_bf16 v[40:43], v[204:207], v[192:195], v[8:11]
	v_mfma_f32_16x16x32_bf16 v[8:11], v[208:211], v[188:191], v[196:199]
	v_mfma_f32_16x16x32_bf16 v[44:47], v[212:215], v[192:195], v[8:11]
	v_mfma_f32_16x16x32_bf16 v[8:11], v[184:187], v[220:223], v[236:239]
	v_mfma_f32_16x16x32_bf16 v[24:27], v[204:207], v[224:227], v[8:11]
	v_mfma_f32_16x16x32_bf16 v[8:11], v[208:211], v[220:223], v[200:203]
	v_mfma_f32_16x16x32_bf16 v[28:31], v[212:215], v[224:227], v[8:11]
	v_mfma_f32_16x16x32_bf16 v[8:11], v[184:187], v[240:243], v[156:159]
	v_mfma_f32_16x16x32_bf16 v[12:15], v[208:211], v[240:243], v[176:179]
	v_mfma_f32_16x16x32_bf16 v[8:11], v[204:207], v[244:247], v[8:11]
	v_mfma_f32_16x16x32_bf16 v[12:15], v[212:215], v[244:247], v[12:15]
	s_setprio 0
.Lmsk_49:
	s_barrier
	s_andn2_b64 vcc, exec, s[16:17]
	s_cbranch_vccnz .LBB0_1070
	s_barrier

.LBB0_4337:
	s_or_b64 exec, exec, s[12:13]
	v_and_b32_e32 v10, 32, v8
	v_bitop3_b32 v10, v2, v10, 48 bitop3:0x6c
	v_and_or_b32 v150, v0, 64, v10
	v_lshlrev_b32_e32 v0, 1, v9
	v_lshrrev_b32_e32 v2, 9, v2
	v_or_b32_e32 v138, v3, v150
	v_and_b32_e32 v0, 24, v0
	v_and_b32_e32 v2, 4, v2
	v_and_b32_e32 v3, 3, v9
	s_ashr_i32 s18, s20, 6
	v_or3_b32 v0, v2, v3, v0
	s_mov_b32 s12, 0x1fffe0
	s_lshl_b32 s29, s18, 10
	v_and_or_b32 v1, v1, s12, v0
	s_add_i32 s49, s29, 0
	v_lshl_or_b32 v128, v1, 11, v150
	s_add_i32 m0, s49, 0x10000
	s_ashr_i32 s21, s20, 8
	v_and_or_b32 v0, v5, s12, v0
	global_load_lds_dwordx4 v128, s[36:37]
	s_add_i32 m0, s49, 0x12000
	v_lshl_or_b32 v130, v0, 11, v150
	s_add_u32 s12, s36, 0x40000
	global_load_lds_dwordx4 v130, s[36:37]
	s_addc_u32 s13, s37, 0
	s_add_i32 m0, s49, 0x14000
	s_add_i32 s50, s49, 0x2000
	global_load_lds_dwordx4 v128, s[12:13]
	s_add_i32 m0, s49, 0x16000
	v_or_b32_e32 v136, v4, v150
	global_load_lds_dwordx4 v130, s[12:13]
	s_mov_b32 m0, s49
	s_add_i32 s51, s49, 0x4000
	global_load_lds_dwordx4 v138, s[30:31]
	s_mov_b32 m0, s50
	v_or_b32_e32 v134, v7, v150
	global_load_lds_dwordx4 v136, s[30:31]
	s_mov_b32 m0, s51
	s_add_i32 s52, s49, 0x6000
	v_or_b32_e32 v140, v6, v150
	global_load_lds_dwordx4 v134, s[30:31]
	s_mov_b32 m0, s52
	v_mov_b32_e32 v133, 0
	global_load_lds_dwordx4 v140, s[30:31]
	v_mov_b32_e32 v129, v133
	v_mov_b32_e32 v131, v133
	v_mov_b32_e32 v139, v133
	v_mov_b32_e32 v137, v133
	s_cmp_eq_u32 s21, 1
	s_mov_b32 s53, 0
	v_lshl_add_u64 v[6:7], s[36:37], 0, v[128:129]
	v_lshl_add_u64 v[4:5], s[36:37], 0, v[130:131]
	v_lshl_add_u64 v[0:1], s[30:31], 0, v[138:139]
	s_cselect_b64 s[12:13], -1, 0
	s_and_b32 s81, s12, 64
	s_add_i32 s82, s81, 0x80
	s_cmp_lg_u32 s21, 1
	v_lshl_add_u64 v[2:3], s[30:31], 0, v[136:137]
	s_cbranch_scc1 .LBB0_4339
	s_barrier

.LBB0_4355:
	ds_read_b128 v[160:163], v152
	ds_read_b128 v[164:167], v152 offset:1024
	ds_read_b128 v[168:171], v152 offset:2048
	ds_read_b128 v[172:175], v152 offset:3072
	ds_read_b128 v[176:179], v153
	ds_read_b128 v[180:183], v153 offset:1024
	ds_read_b128 v[184:187], v153 offset:2048
	ds_read_b128 v[188:191], v153 offset:3072
	s_add_u32 s38, s30, s36
	s_addc_u32 s39, s31, s37
	s_add_u32 s40, s38, 0x100
	s_addc_u32 s41, s39, 0
	s_add_u32 s67, s23, s36
	s_addc_u32 s68, s65, s37
	s_cmpk_eq_i32 s36, 0x700
	s_cselect_b64 vcc, -1, 0
	s_and_b64 s[38:39], vcc, exec
	v_cndmask_b32_e32 v132, v138, v157, vcc
	s_cselect_b32 s41, s27, s41
	s_cselect_b32 s40, s26, s40
	v_cndmask_b32_e32 v224, v136, v156, vcc
	v_cndmask_b32_e32 v135, v134, v155, vcc
	v_cndmask_b32_e32 v141, v140, v158, vcc
	s_cselect_b32 s39, s25, s68
	s_cselect_b32 s38, s24, s67
	s_mov_b32 m0, s59
	v_lshl_add_u64 v[226:227], v[144:145], 0, s[36:37]
	ds_read_b128 v[192:195], v154
	ds_read_b128 v[196:199], v154 offset:1024
	ds_read_b128 v[200:203], v154 offset:2048
	ds_read_b128 v[204:207], v154 offset:3072
	ds_read_b128 v[208:211], v154 offset:4096
	ds_read_b128 v[212:215], v154 offset:5120
	ds_read_b128 v[216:219], v154 offset:6144
	ds_read_b128 v[220:223], v154 offset:7168
	global_load_lds_dwordx4 v[226:227], off
	v_lshl_add_u64 v[226:227], v[142:143], 0, s[36:37]
	s_add_i32 m0, s49, 0xe000
	s_nop 0
	global_load_lds_dwordx4 v[226:227], off
	s_waitcnt vmcnt(8)
	s_waitcnt lgkmcnt(0)
	s_barrier
	s_cmp_le_i32 s80, s81
	s_cbranch_scc1 .Lmsk_16
	s_setprio 1
	s_waitcnt lgkmcnt(0)
	v_mfma_f32_16x16x32_bf16 v[116:119], v[160:163], v[192:195], v[116:119]
	v_mfma_f32_16x16x32_bf16 v[112:115], v[168:171], v[192:195], v[112:115]
	v_mfma_f32_16x16x32_bf16 v[108:111], v[160:163], v[200:203], v[108:111]
	v_mfma_f32_16x16x32_bf16 v[104:107], v[168:171], v[200:203], v[104:107]
	v_mfma_f32_16x16x32_bf16 v[92:95], v[160:163], v[208:211], v[92:95]
	v_mfma_f32_16x16x32_bf16 v[88:91], v[168:171], v[208:211], v[88:91]
	v_mfma_f32_16x16x32_bf16 v[76:79], v[160:163], v[216:219], v[76:79]
	v_mfma_f32_16x16x32_bf16 v[72:75], v[168:171], v[216:219], v[72:75]
	v_mfma_f32_16x16x32_bf16 v[116:119], v[164:167], v[196:199], v[116:119]
	v_mfma_f32_16x16x32_bf16 v[112:115], v[172:175], v[196:199], v[112:115]
	v_mfma_f32_16x16x32_bf16 v[108:111], v[164:167], v[204:207], v[108:111]
	v_mfma_f32_16x16x32_bf16 v[104:107], v[172:175], v[204:207], v[104:107]
	v_mfma_f32_16x16x32_bf16 v[92:95], v[164:167], v[212:215], v[92:95]
	v_mfma_f32_16x16x32_bf16 v[88:91], v[172:175], v[212:215], v[88:91]
	v_mfma_f32_16x16x32_bf16 v[76:79], v[164:167], v[220:223], v[76:79]
	v_mfma_f32_16x16x32_bf16 v[72:75], v[172:175], v[220:223], v[72:75]
	s_setprio 0
	s_setprio 1
	v_mfma_f32_16x16x32_bf16 v[124:127], v[176:179], v[192:195], v[124:127]
	v_mfma_f32_16x16x32_bf16 v[120:123], v[184:187], v[192:195], v[120:123]
	v_mfma_f32_16x16x32_bf16 v[100:103], v[176:179], v[200:203], v[100:103]
	v_mfma_f32_16x16x32_bf16 v[96:99], v[184:187], v[200:203], v[96:99]
	v_mfma_f32_16x16x32_bf16 v[84:87], v[176:179], v[208:211], v[84:87]
	v_mfma_f32_16x16x32_bf16 v[80:83], v[184:187], v[208:211], v[80:83]
	v_mfma_f32_16x16x32_bf16 v[68:71], v[176:179], v[216:219], v[68:71]
	v_mfma_f32_16x16x32_bf16 v[64:67], v[184:187], v[216:219], v[64:67]
	v_mfma_f32_16x16x32_bf16 v[124:127], v[180:183], v[196:199], v[124:127]
	v_mfma_f32_16x16x32_bf16 v[120:123], v[188:191], v[196:199], v[120:123]
	v_mfma_f32_16x16x32_bf16 v[100:103], v[180:183], v[204:207], v[100:103]
	v_mfma_f32_16x16x32_bf16 v[96:99], v[188:191], v[204:207], v[96:99]
	v_mfma_f32_16x16x32_bf16 v[84:87], v[180:183], v[212:215], v[84:87]
	v_mfma_f32_16x16x32_bf16 v[80:83], v[188:191], v[212:215], v[80:83]
	v_mfma_f32_16x16x32_bf16 v[68:71], v[180:183], v[220:223], v[68:71]
	v_mfma_f32_16x16x32_bf16 v[64:67], v[188:191], v[220:223], v[64:67]
	s_setprio 0
.Lmsk_16:
	s_barrier
	s_add_i32 s67, s56, s29
	v_lshl_add_u64 v[226:227], s[38:39], 0, v[128:129]
	s_mov_b32 m0, s67
	ds_read_b128 v[192:195], v154 offset:16384
	ds_read_b128 v[196:199], v154 offset:17408
	ds_read_b128 v[200:203], v154 offset:18432
	ds_read_b128 v[204:207], v154 offset:19456
	ds_read_b128 v[208:211], v154 offset:20480
	ds_read_b128 v[212:215], v154 offset:21504
	ds_read_b128 v[216:219], v154 offset:22528
	ds_read_b128 v[220:223], v154 offset:23552
	global_load_lds_dwordx4 v[226:227], off
	s_add_i32 m0, s67, 0x2000
	s_add_u32 s68, s38, 0x40000
	v_lshl_add_u64 v[228:229], s[38:39], 0, v[130:131]
	s_addc_u32 s69, s39, 0
	s_add_i32 s67, s57, s29
	global_load_lds_dwordx4 v[228:229], off
	v_lshl_add_u64 v[230:231], s[68:69], 0, v[128:129]
	s_mov_b32 m0, s67
	v_mov_b32_e32 v225, v133
	global_load_lds_dwordx4 v[230:231], off
	v_lshl_add_u64 v[230:231], s[68:69], 0, v[130:131]
	s_add_i32 m0, s67, 0x2000
	s_nop 0
	global_load_lds_dwordx4 v[230:231], off
	s_mov_b32 m0, s49
	v_lshl_add_u64 v[230:231], s[40:41], 0, v[132:133]
	global_load_lds_dwordx4 v132, s[40:41]
	s_mov_b32 m0, s50
	s_nop 0
	global_load_lds_dwordx4 v224, s[40:41]
	s_waitcnt vmcnt(8)
	s_waitcnt lgkmcnt(0)
	v_lshl_add_u64 v[224:225], s[40:41], 0, v[224:225]
	s_barrier
	s_cmp_le_i32 s80, s82
	s_cbranch_scc1 .Lmsk_15
	s_setprio 1
	s_waitcnt lgkmcnt(0)
	v_mfma_f32_16x16x32_bf16 v[60:63], v[160:163], v[192:195], v[60:63]
	v_mfma_f32_16x16x32_bf16 v[56:59], v[168:171], v[192:195], v[56:59]
	v_mfma_f32_16x16x32_bf16 v[44:47], v[160:163], v[200:203], v[44:47]
	v_mfma_f32_16x16x32_bf16 v[40:43], v[168:171], v[200:203], v[40:43]
	v_mfma_f32_16x16x32_bf16 v[28:31], v[160:163], v[208:211], v[28:31]
	v_mfma_f32_16x16x32_bf16 v[24:27], v[168:171], v[208:211], v[24:27]
	v_mfma_f32_16x16x32_bf16 v[12:15], v[160:163], v[216:219], v[12:15]
	v_mfma_f32_16x16x32_bf16 v[8:11], v[168:171], v[216:219], v[8:11]
	v_mfma_f32_16x16x32_bf16 v[60:63], v[164:167], v[196:199], v[60:63]
	v_mfma_f32_16x16x32_bf16 v[56:59], v[172:175], v[196:199], v[56:59]
	v_mfma_f32_16x16x32_bf16 v[44:47], v[164:167], v[204:207], v[44:47]
	v_mfma_f32_16x16x32_bf16 v[40:43], v[172:175], v[204:207], v[40:43]
	v_mfma_f32_16x16x32_bf16 v[28:31], v[164:167], v[212:215], v[28:31]
	v_mfma_f32_16x16x32_bf16 v[24:27], v[172:175], v[212:215], v[24:27]
	v_mfma_f32_16x16x32_bf16 v[12:15], v[164:167], v[220:223], v[12:15]
	v_mfma_f32_16x16x32_bf16 v[8:11], v[172:175], v[220:223], v[8:11]
	s_setprio 0
	s_setprio 1
	v_mfma_f32_16x16x32_bf16 v[52:55], v[176:179], v[192:195], v[52:55]
	v_mfma_f32_16x16x32_bf16 v[48:51], v[184:187], v[192:195], v[48:51]
	v_mfma_f32_16x16x32_bf16 v[36:39], v[176:179], v[200:203], v[36:39]
	v_mfma_f32_16x16x32_bf16 v[32:35], v[184:187], v[200:203], v[32:35]
	v_mfma_f32_16x16x32_bf16 v[20:23], v[176:179], v[208:211], v[20:23]
	v_mfma_f32_16x16x32_bf16 v[16:19], v[184:187], v[208:211], v[16:19]
	v_mfma_f32_16x16x32_bf16 v[4:7], v[176:179], v[216:219], v[4:7]
	v_mfma_f32_16x16x32_bf16 v[0:3], v[184:187], v[216:219], v[0:3]
	v_mfma_f32_16x16x32_bf16 v[52:55], v[180:183], v[196:199], v[52:55]
	v_mfma_f32_16x16x32_bf16 v[48:51], v[188:191], v[196:199], v[48:51]
	v_mfma_f32_16x16x32_bf16 v[36:39], v[180:183], v[204:207], v[36:39]
	v_mfma_f32_16x16x32_bf16 v[32:35], v[188:191], v[204:207], v[32:35]
	v_mfma_f32_16x16x32_bf16 v[20:23], v[180:183], v[212:215], v[20:23]
	v_mfma_f32_16x16x32_bf16 v[16:19], v[188:191], v[212:215], v[16:19]
	v_mfma_f32_16x16x32_bf16 v[4:7], v[180:183], v[220:223], v[4:7]
	v_mfma_f32_16x16x32_bf16 v[0:3], v[188:191], v[220:223], v[0:3]
	s_setprio 0
.Lmsk_15:
	s_barrier
	s_add_i32 s67, 0, 0x18000
	v_add_u32_e32 v132, s67, v139
	s_add_i32 s68, 0, 0x1c000
	ds_read_b128 v[160:163], v132
	ds_read_b128 v[164:167], v132 offset:1024
	ds_read_b128 v[168:171], v132 offset:2048
	ds_read_b128 v[172:175], v132 offset:3072
	v_add_u32_e32 v132, s68, v139
	ds_read_b128 v[176:179], v132
	ds_read_b128 v[180:183], v132 offset:1024
	ds_read_b128 v[184:187], v132 offset:2048
	ds_read_b128 v[188:191], v132 offset:3072
	s_mov_b32 m0, s51
	ds_read_b128 v[192:195], v154 offset:32768
	ds_read_b128 v[196:199], v154 offset:33792
	ds_read_b128 v[200:203], v154 offset:34816
	ds_read_b128 v[204:207], v154 offset:35840
	ds_read_b128 v[208:211], v154 offset:36864
	ds_read_b128 v[212:215], v154 offset:37888
	ds_read_b128 v[216:219], v154 offset:38912
	ds_read_b128 v[220:223], v154 offset:39936
	global_load_lds_dwordx4 v135, s[40:41]
	s_mov_b32 m0, s52
	s_nop 0
	global_load_lds_dwordx4 v141, s[40:41]
	s_waitcnt vmcnt(8)
	s_waitcnt lgkmcnt(0)
	s_barrier
	s_cmp_le_i32 s80, s81
	s_cbranch_scc1 .Lmsk_14
	s_setprio 1
	s_waitcnt lgkmcnt(0)
	v_mfma_f32_16x16x32_bf16 v[116:119], v[160:163], v[192:195], v[116:119]
	v_mfma_f32_16x16x32_bf16 v[112:115], v[168:171], v[192:195], v[112:115]
	v_mfma_f32_16x16x32_bf16 v[108:111], v[160:163], v[200:203], v[108:111]
	v_mfma_f32_16x16x32_bf16 v[104:107], v[168:171], v[200:203], v[104:107]
	v_mfma_f32_16x16x32_bf16 v[92:95], v[160:163], v[208:211], v[92:95]
	v_mfma_f32_16x16x32_bf16 v[88:91], v[168:171], v[208:211], v[88:91]
	v_mfma_f32_16x16x32_bf16 v[76:79], v[160:163], v[216:219], v[76:79]
	v_mfma_f32_16x16x32_bf16 v[72:75], v[168:171], v[216:219], v[72:75]
	v_mfma_f32_16x16x32_bf16 v[116:119], v[164:167], v[196:199], v[116:119]
	v_mfma_f32_16x16x32_bf16 v[112:115], v[172:175], v[196:199], v[112:115]
	v_mfma_f32_16x16x32_bf16 v[108:111], v[164:167], v[204:207], v[108:111]
	v_mfma_f32_16x16x32_bf16 v[104:107], v[172:175], v[204:207], v[104:107]
	v_mfma_f32_16x16x32_bf16 v[92:95], v[164:167], v[212:215], v[92:95]
	v_mfma_f32_16x16x32_bf16 v[88:91], v[172:175], v[212:215], v[88:91]
	v_mfma_f32_16x16x32_bf16 v[76:79], v[164:167], v[220:223], v[76:79]
	v_mfma_f32_16x16x32_bf16 v[72:75], v[172:175], v[220:223], v[72:75]
	s_setprio 0
	s_setprio 1
	v_mfma_f32_16x16x32_bf16 v[124:127], v[176:179], v[192:195], v[124:127]
	v_mfma_f32_16x16x32_bf16 v[120:123], v[184:187], v[192:195], v[120:123]
	v_mfma_f32_16x16x32_bf16 v[100:103], v[176:179], v[200:203], v[100:103]
	v_mfma_f32_16x16x32_bf16 v[96:99], v[184:187], v[200:203], v[96:99]
	v_mfma_f32_16x16x32_bf16 v[84:87], v[176:179], v[208:211], v[84:87]
	v_mfma_f32_16x16x32_bf16 v[80:83], v[184:187], v[208:211], v[80:83]
	v_mfma_f32_16x16x32_bf16 v[68:71], v[176:179], v[216:219], v[68:71]
	v_mfma_f32_16x16x32_bf16 v[64:67], v[184:187], v[216:219], v[64:67]
	v_mfma_f32_16x16x32_bf16 v[124:127], v[180:183], v[196:199], v[124:127]
	v_mfma_f32_16x16x32_bf16 v[120:123], v[188:191], v[196:199], v[120:123]
	v_mfma_f32_16x16x32_bf16 v[100:103], v[180:183], v[204:207], v[100:103]
	v_mfma_f32_16x16x32_bf16 v[96:99], v[188:191], v[204:207], v[96:99]
	v_mfma_f32_16x16x32_bf16 v[84:87], v[180:183], v[212:215], v[84:87]
	v_mfma_f32_16x16x32_bf16 v[80:83], v[188:191], v[212:215], v[80:83]
	v_mfma_f32_16x16x32_bf16 v[68:71], v[180:183], v[220:223], v[68:71]
	v_mfma_f32_16x16x32_bf16 v[64:67], v[188:191], v[220:223], v[64:67]
	s_setprio 0
.Lmsk_14:
	s_barrier
	s_add_i32 s40, s67, s29
	v_lshl_add_u64 v[226:227], v[226:227], 0, s[18:19]
	s_mov_b32 m0, s40
	ds_read_b128 v[192:195], v154 offset:49152
	ds_read_b128 v[196:199], v154 offset:50176
	ds_read_b128 v[200:203], v154 offset:51200
	ds_read_b128 v[204:207], v154 offset:52224
	ds_read_b128 v[208:211], v154 offset:53248
	ds_read_b128 v[212:215], v154 offset:54272
	ds_read_b128 v[216:219], v154 offset:55296
	ds_read_b128 v[220:223], v154 offset:56320
	global_load_lds_dwordx4 v[226:227], off
	s_add_i32 m0, s40, 0x2000
	s_add_u32 s38, s38, 0x40080
	v_lshl_add_u64 v[226:227], v[228:229], 0, s[18:19]
	s_addc_u32 s39, s39, 0
	s_add_i32 s40, s68, s29
	global_load_lds_dwordx4 v[226:227], off
	v_lshl_add_u64 v[226:227], s[38:39], 0, v[128:129]
	s_mov_b32 m0, s40
	v_lshl_add_u64 v[224:225], v[224:225], 0, s[18:19]
	global_load_lds_dwordx4 v[226:227], off
	v_lshl_add_u64 v[226:227], s[38:39], 0, v[130:131]
	s_add_i32 m0, s40, 0x2000
	s_nop 0
	global_load_lds_dwordx4 v[226:227], off
	v_lshl_add_u64 v[226:227], v[230:231], 0, s[18:19]
	s_mov_b32 m0, s54
	s_nop 0
	global_load_lds_dwordx4 v[226:227], off
	s_mov_b32 m0, s55
	s_nop 0
	global_load_lds_dwordx4 v[224:225], off
	s_waitcnt vmcnt(8)
	s_waitcnt lgkmcnt(0)
	s_barrier
	s_cmp_le_i32 s80, s82
	s_cbranch_scc1 .Lmsk_13
	s_setprio 1
	s_waitcnt lgkmcnt(0)
	v_mfma_f32_16x16x32_bf16 v[60:63], v[160:163], v[192:195], v[60:63]
	v_mfma_f32_16x16x32_bf16 v[56:59], v[168:171], v[192:195], v[56:59]
	v_mfma_f32_16x16x32_bf16 v[44:47], v[160:163], v[200:203], v[44:47]
	v_mfma_f32_16x16x32_bf16 v[40:43], v[168:171], v[200:203], v[40:43]
	v_mfma_f32_16x16x32_bf16 v[28:31], v[160:163], v[208:211], v[28:31]
	v_mfma_f32_16x16x32_bf16 v[24:27], v[168:171], v[208:211], v[24:27]
	v_mfma_f32_16x16x32_bf16 v[12:15], v[160:163], v[216:219], v[12:15]
	v_mfma_f32_16x16x32_bf16 v[8:11], v[168:171], v[216:219], v[8:11]
	v_mfma_f32_16x16x32_bf16 v[60:63], v[164:167], v[196:199], v[60:63]
	v_mfma_f32_16x16x32_bf16 v[56:59], v[172:175], v[196:199], v[56:59]
	v_mfma_f32_16x16x32_bf16 v[44:47], v[164:167], v[204:207], v[44:47]
	v_mfma_f32_16x16x32_bf16 v[40:43], v[172:175], v[204:207], v[40:43]
	v_mfma_f32_16x16x32_bf16 v[28:31], v[164:167], v[212:215], v[28:31]
	v_mfma_f32_16x16x32_bf16 v[24:27], v[172:175], v[212:215], v[24:27]
	v_mfma_f32_16x16x32_bf16 v[12:15], v[164:167], v[220:223], v[12:15]
	v_mfma_f32_16x16x32_bf16 v[8:11], v[172:175], v[220:223], v[8:11]
	s_setprio 0
	s_setprio 1
	v_mfma_f32_16x16x32_bf16 v[52:55], v[176:179], v[192:195], v[52:55]
	v_mfma_f32_16x16x32_bf16 v[48:51], v[184:187], v[192:195], v[48:51]
	v_mfma_f32_16x16x32_bf16 v[36:39], v[176:179], v[200:203], v[36:39]
	v_mfma_f32_16x16x32_bf16 v[32:35], v[184:187], v[200:203], v[32:35]
	v_mfma_f32_16x16x32_bf16 v[20:23], v[176:179], v[208:211], v[20:23]
	v_mfma_f32_16x16x32_bf16 v[16:19], v[184:187], v[208:211], v[16:19]
	v_mfma_f32_16x16x32_bf16 v[4:7], v[176:179], v[216:219], v[4:7]
	v_mfma_f32_16x16x32_bf16 v[0:3], v[184:187], v[216:219], v[0:3]
	v_mfma_f32_16x16x32_bf16 v[52:55], v[180:183], v[196:199], v[52:55]
	v_mfma_f32_16x16x32_bf16 v[48:51], v[188:191], v[196:199], v[48:51]
	v_mfma_f32_16x16x32_bf16 v[36:39], v[180:183], v[204:207], v[36:39]
	v_mfma_f32_16x16x32_bf16 v[32:35], v[188:191], v[204:207], v[32:35]
	v_mfma_f32_16x16x32_bf16 v[20:23], v[180:183], v[212:215], v[20:23]
	v_mfma_f32_16x16x32_bf16 v[16:19], v[188:191], v[212:215], v[16:19]
	v_mfma_f32_16x16x32_bf16 v[4:7], v[180:183], v[220:223], v[4:7]
	v_mfma_f32_16x16x32_bf16 v[0:3], v[188:191], v[220:223], v[0:3]
	s_setprio 0
.Lmsk_13:
	s_barrier
	s_add_i32 s66, s66, 2
	s_add_u32 s36, s36, 0x100
	s_addc_u32 s37, s37, 0
	s_cmp_gt_u32 s66, 13
	s_cbranch_scc0 .LBB0_4355
	s_and_b64 vcc, exec, s[20:21]
	s_cbranch_vccz .LBB0_4358
	s_barrier

.LBB0_4452:
	v_lshlrev_b32_e32 v1, 4, v0
	v_and_b32_e32 v2, 32, v8
	v_bitop3_b32 v2, v1, v2, 48 bitop3:0x6c
	v_lshrrev_b32_e32 v5, 1, v0
	v_lshrrev_b32_e32 v2, 1, v2
	v_bfe_u32 v3, v0, 2, 26
	v_bfe_u32 v4, v1, 6, 4
	v_and_or_b32 v2, v5, 32, v2
	v_and_b32_e32 v5, 48, v0
	v_lshrrev_b32_e32 v6, 5, v0
	v_lshrrev_b32_e32 v0, 3, v0
	s_mov_b32 s4, 0x1fffff0
	v_and_b32_e32 v6, 4, v6
	v_bfe_u32 v7, v1, 6, 2
	v_and_or_b32 v0, v0, s4, v4
	s_movk_i32 s6, 0x180
	v_or3_b32 v5, v7, v6, v5
	s_movk_i32 s5, 0xc0
	v_mul_lo_u32 v0, v0, s6
	v_and_or_b32 v3, v3, s5, v5
	v_or_b32_e32 v0, v0, v2
	v_lshlrev_b32_e32 v128, 1, v0
	v_mul_u32_u24_e32 v0, 0x180, v3
	v_or_b32_e32 v0, v0, v2
	s_ashr_i32 s14, s16, 6
	v_lshlrev_b32_e32 v130, 1, v0
	v_add_u32_e32 v0, 0x2000, v1
	v_lshrrev_b32_e32 v1, 7, v0
	v_lshrrev_b32_e32 v0, 6, v0
	s_lshl_b32 s45, s14, 10
	v_and_or_b32 v0, v0, s5, v5
	s_add_i32 s46, s45, 0
	v_mul_u32_u24_e32 v0, 0x180, v0
	s_add_i32 m0, s46, 0x10000
	v_or_b32_e32 v0, v0, v2
	s_ashr_i32 s17, s16, 8
	global_load_lds_dwordx4 v130, s[38:39]
	s_add_i32 m0, s46, 0x12000
	v_and_or_b32 v1, v1, s4, v4
	v_lshlrev_b32_e32 v134, 1, v0
	s_add_u32 s4, s38, 0x1800
	global_load_lds_dwordx4 v134, s[38:39]
	s_addc_u32 s5, s39, 0
	s_add_i32 m0, s46, 0x14000
	v_mul_lo_u32 v1, v1, s6
	global_load_lds_dwordx4 v130, s[4:5]
	s_add_i32 m0, s46, 0x16000
	s_add_i32 s47, s46, 0x2000
	v_or_b32_e32 v1, v1, v2
	global_load_lds_dwordx4 v134, s[4:5]
	s_mov_b32 m0, s46
	s_add_u32 s4, s36, 0x18000
	v_lshlrev_b32_e32 v132, 1, v1
	global_load_lds_dwordx4 v128, s[36:37]
	s_mov_b32 m0, s47
	s_addc_u32 s5, s37, 0
	s_add_i32 s49, s46, 0x4000
	global_load_lds_dwordx4 v132, s[36:37]
	s_mov_b32 m0, s49
	s_add_i32 s50, s46, 0x6000
	global_load_lds_dwordx4 v128, s[4:5]
	s_mov_b32 m0, s50
	v_mov_b32_e32 v131, 0
	global_load_lds_dwordx4 v132, s[4:5]
	v_mov_b32_e32 v135, v131
	v_mov_b32_e32 v129, v131
	v_mov_b32_e32 v133, v131
	s_cmp_eq_u32 s17, 1
	v_lshl_add_u64 v[6:7], s[38:39], 0, v[130:131]
	v_lshl_add_u64 v[4:5], s[38:39], 0, v[134:135]
	v_lshl_add_u64 v[0:1], s[36:37], 0, v[128:129]
	s_cselect_b64 s[4:5], -1, 0
	s_and_b32 s81, s4, 64
	s_add_i32 s82, s81, 0x80
	s_cmp_lg_u32 s17, 1
	v_lshl_add_u64 v[2:3], s[36:37], 0, v[132:133]
	s_cbranch_scc1 .LBB0_4454
	s_barrier

.LBB0_4459:
	ds_read_b128 v[8:11], v149
	ds_read_b128 v[12:15], v149 offset:1024
	ds_read_b128 v[16:19], v149 offset:2048
	ds_read_b128 v[20:23], v149 offset:3072
	ds_read_b128 v[24:27], v150
	ds_read_b128 v[28:31], v150 offset:1024
	ds_read_b128 v[32:35], v150 offset:2048
	ds_read_b128 v[36:39], v150 offset:3072
	s_add_u32 s68, s36, 0x18080
	s_addc_u32 s69, s37, 0
	s_mov_b32 m0, s61
	v_lshl_add_u64 v[64:65], s[68:69], 0, v[128:129]
	ds_read_b128 v[0:3], v140
	ds_read_b128 v[4:7], v140 offset:1024
	ds_read_b128 v[40:43], v140 offset:2048
	ds_read_b128 v[44:47], v140 offset:3072
	ds_read_b128 v[48:51], v140 offset:4096
	ds_read_b128 v[52:55], v140 offset:5120
	ds_read_b128 v[56:59], v140 offset:6144
	ds_read_b128 v[60:63], v140 offset:7168
	global_load_lds_dwordx4 v[64:65], off
	v_lshl_add_u64 v[64:65], s[68:69], 0, v[132:133]
	s_mov_b32 m0, s62
	s_nop 0
	global_load_lds_dwordx4 v[64:65], off
	s_waitcnt vmcnt(8)
	s_waitcnt lgkmcnt(0)
	s_barrier
	s_cmp_le_i32 s51, s81
	s_cbranch_scc1 .Lmsk_12
	s_setprio 1
	s_waitcnt lgkmcnt(0)
	v_mfma_f32_16x16x32_bf16 v[64:67], v[8:11], v[0:3], 0
	v_mfma_f32_16x16x32_bf16 v[68:71], v[16:19], v[0:3], 0
	v_mfma_f32_16x16x32_bf16 v[72:75], v[8:11], v[40:43], 0
	v_mfma_f32_16x16x32_bf16 v[76:79], v[16:19], v[40:43], 0
	v_mfma_f32_16x16x32_bf16 v[80:83], v[8:11], v[48:51], 0
	v_mfma_f32_16x16x32_bf16 v[84:87], v[16:19], v[48:51], 0
	v_mfma_f32_16x16x32_bf16 v[88:91], v[8:11], v[56:59], 0
	v_mfma_f32_16x16x32_bf16 v[92:95], v[16:19], v[56:59], 0
	v_mfma_f32_16x16x32_bf16 v[64:67], v[12:15], v[4:7], v[64:67]
	v_mfma_f32_16x16x32_bf16 v[68:71], v[20:23], v[4:7], v[68:71]
	v_mfma_f32_16x16x32_bf16 v[72:75], v[12:15], v[44:47], v[72:75]
	v_mfma_f32_16x16x32_bf16 v[76:79], v[20:23], v[44:47], v[76:79]
	v_mfma_f32_16x16x32_bf16 v[80:83], v[12:15], v[52:55], v[80:83]
	v_mfma_f32_16x16x32_bf16 v[84:87], v[20:23], v[52:55], v[84:87]
	v_mfma_f32_16x16x32_bf16 v[88:91], v[12:15], v[60:63], v[88:91]
	v_mfma_f32_16x16x32_bf16 v[92:95], v[20:23], v[60:63], v[92:95]
	s_setprio 0
	s_setprio 1
	v_mfma_f32_16x16x32_bf16 v[96:99], v[24:27], v[0:3], 0
	v_mfma_f32_16x16x32_bf16 v[0:3], v[32:35], v[0:3], 0
	v_mfma_f32_16x16x32_bf16 v[100:103], v[36:39], v[4:7], v[0:3]
	v_mfma_f32_16x16x32_bf16 v[0:3], v[24:27], v[40:43], 0
	v_mfma_f32_16x16x32_bf16 v[104:107], v[28:31], v[44:47], v[0:3]
	v_mfma_f32_16x16x32_bf16 v[0:3], v[32:35], v[40:43], 0
	v_mfma_f32_16x16x32_bf16 v[40:43], v[36:39], v[44:47], v[0:3]
	v_mfma_f32_16x16x32_bf16 v[0:3], v[24:27], v[48:51], 0
	v_mfma_f32_16x16x32_bf16 v[44:47], v[28:31], v[52:55], v[0:3]
	v_mfma_f32_16x16x32_bf16 v[0:3], v[32:35], v[48:51], 0
	v_mfma_f32_16x16x32_bf16 v[48:51], v[36:39], v[52:55], v[0:3]
	v_mfma_f32_16x16x32_bf16 v[0:3], v[24:27], v[56:59], 0
	v_mfma_f32_16x16x32_bf16 v[52:55], v[28:31], v[60:63], v[0:3]
	v_mfma_f32_16x16x32_bf16 v[0:3], v[32:35], v[56:59], 0
	v_mfma_f32_16x16x32_bf16 v[96:99], v[28:31], v[4:7], v[96:99]
	v_mfma_f32_16x16x32_bf16 v[56:59], v[36:39], v[60:63], v[0:3]
	s_setprio 0
.Lmsk_12:
	s_barrier
	s_nop 3
	v_lshl_add_u64 v[0:1], s[38:39], 0, v[130:131]
	s_add_i32 s70, s59, s45
	v_lshl_add_u64 v[2:3], v[0:1], 0, s[18:19]
	s_mov_b32 m0, s70
	s_add_i32 s67, s70, 0x2000
	ds_read_b128 v[60:63], v140 offset:16384
	ds_read_b128 v[108:111], v140 offset:17408
	ds_read_b128 v[112:115], v140 offset:18432
	ds_read_b128 v[116:119], v140 offset:19456
	ds_read_b128 v[120:123], v140 offset:20480
	ds_read_b128 v[124:127], v140 offset:21504
	ds_read_b128 v[152:155], v140 offset:22528
	ds_read_b128 v[156:159], v140 offset:23552
	global_load_lds_dwordx4 v[2:3], off
	v_lshl_add_u64 v[2:3], s[38:39], 0, v[134:135]
	s_add_u32 s72, s38, 0x1900
	v_lshl_add_u64 v[4:5], v[2:3], 0, s[18:19]
	s_mov_b32 m0, s67
	s_addc_u32 s73, s39, 0
	s_add_i32 s68, s60, s45
	global_load_lds_dwordx4 v[4:5], off
	v_lshl_add_u64 v[4:5], s[72:73], 0, v[130:131]
	s_mov_b32 m0, s68
	s_add_i32 s69, s68, 0x2000
	global_load_lds_dwordx4 v[4:5], off
	v_lshl_add_u64 v[4:5], s[72:73], 0, v[134:135]
	s_mov_b32 m0, s69
	s_nop 0
	global_load_lds_dwordx4 v[4:5], off
	v_lshl_add_u64 v[4:5], s[36:37], 0, v[128:129]
	v_lshl_add_u64 v[6:7], v[4:5], 0, s[18:19]
	s_mov_b32 m0, s46
	s_nop 0
	global_load_lds_dwordx4 v[6:7], off
	v_lshl_add_u64 v[6:7], s[36:37], 0, v[132:133]
	v_lshl_add_u64 v[136:137], v[6:7], 0, s[18:19]
	s_mov_b32 m0, s47
	s_nop 0
	global_load_lds_dwordx4 v[136:137], off
	s_waitcnt vmcnt(8)
	s_waitcnt lgkmcnt(0)
	s_barrier
	s_cmp_le_i32 s51, s82
	s_cbranch_scc1 .Lmsk_11
	s_setprio 1
	s_waitcnt lgkmcnt(0)
	v_mfma_f32_16x16x32_bf16 v[160:163], v[8:11], v[60:63], 0
	v_mfma_f32_16x16x32_bf16 v[168:171], v[8:11], v[112:115], 0
	v_mfma_f32_16x16x32_bf16 v[176:179], v[8:11], v[120:123], 0
	v_mfma_f32_16x16x32_bf16 v[8:11], v[8:11], v[152:155], 0
	v_mfma_f32_16x16x32_bf16 v[160:163], v[12:15], v[108:111], v[160:163]
	v_mfma_f32_16x16x32_bf16 v[164:167], v[16:19], v[60:63], 0
	v_mfma_f32_16x16x32_bf16 v[168:171], v[12:15], v[116:119], v[168:171]
	v_mfma_f32_16x16x32_bf16 v[172:175], v[16:19], v[112:115], 0
	v_mfma_f32_16x16x32_bf16 v[176:179], v[12:15], v[124:127], v[176:179]
	v_mfma_f32_16x16x32_bf16 v[180:183], v[16:19], v[120:123], 0
	v_mfma_f32_16x16x32_bf16 v[10:13], v[12:15], v[156:159], v[8:11]
	v_mfma_f32_16x16x32_bf16 v[14:17], v[16:19], v[152:155], 0
	v_mfma_f32_16x16x32_bf16 v[14:17], v[20:23], v[156:159], v[14:17]
	v_mfma_f32_16x16x32_bf16 v[164:167], v[20:23], v[108:111], v[164:167]
	v_mfma_f32_16x16x32_bf16 v[172:175], v[20:23], v[116:119], v[172:175]
	v_mfma_f32_16x16x32_bf16 v[180:183], v[20:23], v[124:127], v[180:183]
	s_setprio 0
	s_setprio 1
	v_mfma_f32_16x16x32_bf16 v[18:21], v[24:27], v[60:63], 0
	v_mfma_f32_16x16x32_bf16 v[60:63], v[32:35], v[60:63], 0
	v_mfma_f32_16x16x32_bf16 v[18:21], v[28:31], v[108:111], v[18:21]
	v_mfma_f32_16x16x32_bf16 v[60:63], v[36:39], v[108:111], v[60:63]
	v_mfma_f32_16x16x32_bf16 v[108:111], v[24:27], v[112:115], 0
	v_mfma_f32_16x16x32_bf16 v[112:115], v[32:35], v[112:115], 0
	v_mfma_f32_16x16x32_bf16 v[108:111], v[28:31], v[116:119], v[108:111]
	v_mfma_f32_16x16x32_bf16 v[112:115], v[36:39], v[116:119], v[112:115]
	v_mfma_f32_16x16x32_bf16 v[116:119], v[24:27], v[120:123], 0
	v_mfma_f32_16x16x32_bf16 v[22:25], v[24:27], v[152:155], 0
	v_mfma_f32_16x16x32_bf16 v[116:119], v[28:31], v[124:127], v[116:119]
	v_mfma_f32_16x16x32_bf16 v[120:123], v[32:35], v[120:123], 0
	v_mfma_f32_16x16x32_bf16 v[22:25], v[28:31], v[156:159], v[22:25]
	v_mfma_f32_16x16x32_bf16 v[26:29], v[32:35], v[152:155], 0
	v_mfma_f32_16x16x32_bf16 v[120:123], v[36:39], v[124:127], v[120:123]
	v_mfma_f32_16x16x32_bf16 v[26:29], v[36:39], v[156:159], v[26:29]
	s_setprio 0
.Lmsk_11:
	s_barrier
	s_add_i32 s74, 0, 0x18000
	s_add_i32 s75, 0, 0x1c000
	v_add_u32_e32 v8, s74, v139
	v_add_u32_e32 v9, s75, v139
	ds_read_b128 v[30:33], v8
	ds_read_b128 v[34:37], v8 offset:1024
	ds_read_b128 v[124:127], v8 offset:2048
	ds_read_b128 v[152:155], v8 offset:3072
	ds_read_b128 v[156:159], v9
	ds_read_b128 v[184:187], v9 offset:1024
	ds_read_b128 v[188:191], v9 offset:2048
	ds_read_b128 v[192:195], v9 offset:3072
	s_add_u32 s72, s36, 0x18100
	s_addc_u32 s73, s37, 0
	s_mov_b32 m0, s49
	v_lshl_add_u64 v[38:39], s[72:73], 0, v[128:129]
	ds_read_b128 v[196:199], v140 offset:32768
	ds_read_b128 v[200:203], v140 offset:33792
	ds_read_b128 v[204:207], v140 offset:34816
	ds_read_b128 v[208:211], v140 offset:35840
	ds_read_b128 v[212:215], v140 offset:36864
	ds_read_b128 v[216:219], v140 offset:37888
	ds_read_b128 v[220:223], v140 offset:38912
	ds_read_b128 v[224:227], v140 offset:39936
	global_load_lds_dwordx4 v[38:39], off
	v_lshl_add_u64 v[38:39], s[72:73], 0, v[132:133]
	s_mov_b32 m0, s50
	s_nop 0
	global_load_lds_dwordx4 v[38:39], off
	s_waitcnt vmcnt(8)
	s_waitcnt lgkmcnt(0)
	s_barrier
	s_cmp_le_i32 s51, s81
	s_cbranch_scc1 .Lmsk_10
	s_setprio 1
	s_waitcnt lgkmcnt(0)
	v_mfma_f32_16x16x32_bf16 v[64:67], v[30:33], v[196:199], v[64:67]
	v_mfma_f32_16x16x32_bf16 v[68:71], v[124:127], v[196:199], v[68:71]
	v_mfma_f32_16x16x32_bf16 v[72:75], v[30:33], v[204:207], v[72:75]
	v_mfma_f32_16x16x32_bf16 v[76:79], v[124:127], v[204:207], v[76:79]
	v_mfma_f32_16x16x32_bf16 v[80:83], v[30:33], v[212:215], v[80:83]
	v_mfma_f32_16x16x32_bf16 v[84:87], v[124:127], v[212:215], v[84:87]
	v_mfma_f32_16x16x32_bf16 v[88:91], v[30:33], v[220:223], v[88:91]
	v_mfma_f32_16x16x32_bf16 v[92:95], v[124:127], v[220:223], v[92:95]
	v_mfma_f32_16x16x32_bf16 v[64:67], v[34:37], v[200:203], v[64:67]
	v_mfma_f32_16x16x32_bf16 v[68:71], v[152:155], v[200:203], v[68:71]
	v_mfma_f32_16x16x32_bf16 v[72:75], v[34:37], v[208:211], v[72:75]
	v_mfma_f32_16x16x32_bf16 v[76:79], v[152:155], v[208:211], v[76:79]
	v_mfma_f32_16x16x32_bf16 v[80:83], v[34:37], v[216:219], v[80:83]
	v_mfma_f32_16x16x32_bf16 v[84:87], v[152:155], v[216:219], v[84:87]
	v_mfma_f32_16x16x32_bf16 v[88:91], v[34:37], v[224:227], v[88:91]
	v_mfma_f32_16x16x32_bf16 v[92:95], v[152:155], v[224:227], v[92:95]
	s_setprio 0
	s_setprio 1
	v_mfma_f32_16x16x32_bf16 v[96:99], v[156:159], v[196:199], v[96:99]
	v_mfma_f32_16x16x32_bf16 v[100:103], v[188:191], v[196:199], v[100:103]
	v_mfma_f32_16x16x32_bf16 v[104:107], v[156:159], v[204:207], v[104:107]
	v_mfma_f32_16x16x32_bf16 v[38:41], v[188:191], v[204:207], v[40:43]
	v_mfma_f32_16x16x32_bf16 v[42:45], v[156:159], v[212:215], v[44:47]
	v_mfma_f32_16x16x32_bf16 v[46:49], v[188:191], v[212:215], v[48:51]
	v_mfma_f32_16x16x32_bf16 v[50:53], v[156:159], v[220:223], v[52:55]
	v_mfma_f32_16x16x32_bf16 v[54:57], v[188:191], v[220:223], v[56:59]
	v_mfma_f32_16x16x32_bf16 v[96:99], v[184:187], v[200:203], v[96:99]
	v_mfma_f32_16x16x32_bf16 v[100:103], v[192:195], v[200:203], v[100:103]
	v_mfma_f32_16x16x32_bf16 v[104:107], v[184:187], v[208:211], v[104:107]
	v_mfma_f32_16x16x32_bf16 v[38:41], v[192:195], v[208:211], v[38:41]
	v_mfma_f32_16x16x32_bf16 v[42:45], v[184:187], v[216:219], v[42:45]
	v_mfma_f32_16x16x32_bf16 v[46:49], v[192:195], v[216:219], v[46:49]
	v_mfma_f32_16x16x32_bf16 v[50:53], v[184:187], v[224:227], v[50:53]
	v_mfma_f32_16x16x32_bf16 v[54:57], v[192:195], v[224:227], v[54:57]
	s_setprio 0
.Lmsk_10:
	s_barrier
	s_add_i32 s74, s74, s45
	s_add_i32 s71, s74, 0x2000
	v_lshl_add_u64 v[58:59], v[0:1], 0, s[20:21]
	s_mov_b32 m0, s74
	s_add_u32 s76, s38, 0x1980
	ds_read_b128 v[196:199], v140 offset:49152
	ds_read_b128 v[200:203], v140 offset:50176
	ds_read_b128 v[204:207], v140 offset:51200
	ds_read_b128 v[208:211], v140 offset:52224
	ds_read_b128 v[212:215], v140 offset:53248
	ds_read_b128 v[216:219], v140 offset:54272
	ds_read_b128 v[220:223], v140 offset:55296
	ds_read_b128 v[224:227], v140 offset:56320
	global_load_lds_dwordx4 v[58:59], off
	v_lshl_add_u64 v[58:59], v[2:3], 0, s[20:21]
	s_mov_b32 m0, s71
	s_addc_u32 s77, s39, 0
	s_add_i32 s72, s75, s45
	global_load_lds_dwordx4 v[58:59], off
	v_lshl_add_u64 v[58:59], s[76:77], 0, v[130:131]
	s_mov_b32 m0, s72
	s_add_i32 s73, s72, 0x2000
	global_load_lds_dwordx4 v[58:59], off
	v_lshl_add_u64 v[58:59], s[76:77], 0, v[134:135]
	s_mov_b32 m0, s73
	s_nop 0
	global_load_lds_dwordx4 v[58:59], off
	v_lshl_add_u64 v[58:59], v[4:5], 0, s[20:21]
	s_mov_b32 m0, s52
	s_nop 0
	global_load_lds_dwordx4 v[58:59], off
	v_lshl_add_u64 v[58:59], v[6:7], 0, s[20:21]
	s_mov_b32 m0, s53
	s_nop 0
	global_load_lds_dwordx4 v[58:59], off
	s_waitcnt vmcnt(8)
	s_waitcnt lgkmcnt(0)
	s_barrier
	s_cmp_le_i32 s51, s82
	s_cbranch_scc1 .Lmsk_9
	s_setprio 1
	s_waitcnt lgkmcnt(0)
	v_mfma_f32_16x16x32_bf16 v[10:13], v[30:33], v[220:223], v[10:13]
	v_mfma_f32_16x16x32_bf16 v[14:17], v[124:127], v[220:223], v[14:17]
	v_mfma_f32_16x16x32_bf16 v[160:163], v[30:33], v[196:199], v[160:163]
	v_mfma_f32_16x16x32_bf16 v[164:167], v[124:127], v[196:199], v[164:167]
	v_mfma_f32_16x16x32_bf16 v[168:171], v[30:33], v[204:207], v[168:171]
	v_mfma_f32_16x16x32_bf16 v[172:175], v[124:127], v[204:207], v[172:175]
	v_mfma_f32_16x16x32_bf16 v[176:179], v[30:33], v[212:215], v[176:179]
	v_mfma_f32_16x16x32_bf16 v[180:183], v[124:127], v[212:215], v[180:183]
	v_mfma_f32_16x16x32_bf16 v[10:13], v[34:37], v[224:227], v[10:13]
	v_mfma_f32_16x16x32_bf16 v[14:17], v[152:155], v[224:227], v[14:17]
	v_mfma_f32_16x16x32_bf16 v[160:163], v[34:37], v[200:203], v[160:163]
	v_mfma_f32_16x16x32_bf16 v[164:167], v[152:155], v[200:203], v[164:167]
	v_mfma_f32_16x16x32_bf16 v[168:171], v[34:37], v[208:211], v[168:171]
	v_mfma_f32_16x16x32_bf16 v[172:175], v[152:155], v[208:211], v[172:175]
	v_mfma_f32_16x16x32_bf16 v[176:179], v[34:37], v[216:219], v[176:179]
	v_mfma_f32_16x16x32_bf16 v[180:183], v[152:155], v[216:219], v[180:183]
	s_setprio 0
	s_setprio 1
	v_mfma_f32_16x16x32_bf16 v[18:21], v[156:159], v[196:199], v[18:21]
	v_mfma_f32_16x16x32_bf16 v[30:33], v[188:191], v[196:199], v[60:63]
	v_mfma_f32_16x16x32_bf16 v[34:37], v[156:159], v[204:207], v[108:111]
	v_mfma_f32_16x16x32_bf16 v[58:61], v[188:191], v[204:207], v[112:115]
	v_mfma_f32_16x16x32_bf16 v[108:111], v[156:159], v[212:215], v[116:119]
	v_mfma_f32_16x16x32_bf16 v[112:115], v[188:191], v[212:215], v[120:123]
	v_mfma_f32_16x16x32_bf16 v[22:25], v[156:159], v[220:223], v[22:25]
	v_mfma_f32_16x16x32_bf16 v[26:29], v[188:191], v[220:223], v[26:29]
	v_mfma_f32_16x16x32_bf16 v[18:21], v[184:187], v[200:203], v[18:21]
	v_mfma_f32_16x16x32_bf16 v[30:33], v[192:195], v[200:203], v[30:33]
	v_mfma_f32_16x16x32_bf16 v[34:37], v[184:187], v[208:211], v[34:37]
	v_mfma_f32_16x16x32_bf16 v[58:61], v[192:195], v[208:211], v[58:61]
	v_mfma_f32_16x16x32_bf16 v[108:111], v[184:187], v[216:219], v[108:111]
	v_mfma_f32_16x16x32_bf16 v[112:115], v[192:195], v[216:219], v[112:115]
	v_mfma_f32_16x16x32_bf16 v[22:25], v[184:187], v[224:227], v[22:25]
	v_mfma_f32_16x16x32_bf16 v[26:29], v[192:195], v[224:227], v[26:29]
	s_setprio 0
.Lmsk_9:
	s_barrier
	ds_read_b128 v[116:119], v149
	ds_read_b128 v[120:123], v149 offset:1024
	ds_read_b128 v[124:127], v149 offset:2048
	ds_read_b128 v[152:155], v149 offset:3072
	ds_read_b128 v[156:159], v150
	ds_read_b128 v[184:187], v150 offset:1024
	ds_read_b128 v[188:191], v150 offset:2048
	ds_read_b128 v[192:195], v150 offset:3072
	s_add_u32 s76, s36, 0x18180
	s_addc_u32 s77, s37, 0
	s_mov_b32 m0, s61
	v_lshl_add_u64 v[62:63], s[76:77], 0, v[128:129]
	ds_read_b128 v[196:199], v140
	ds_read_b128 v[200:203], v140 offset:1024
	ds_read_b128 v[204:207], v140 offset:2048
	ds_read_b128 v[208:211], v140 offset:3072
	ds_read_b128 v[212:215], v140 offset:4096
	ds_read_b128 v[216:219], v140 offset:5120
	ds_read_b128 v[220:223], v140 offset:6144
	ds_read_b128 v[224:227], v140 offset:7168
	global_load_lds_dwordx4 v[62:63], off
	v_lshl_add_u64 v[62:63], s[76:77], 0, v[132:133]
	s_mov_b32 m0, s62
	s_nop 0
	global_load_lds_dwordx4 v[62:63], off
	s_waitcnt vmcnt(8)
	s_waitcnt lgkmcnt(0)
	s_barrier
	s_cmp_le_i32 s51, s81
	s_cbranch_scc1 .Lmsk_8
	s_setprio 1
	s_waitcnt lgkmcnt(0)
	v_mfma_f32_16x16x32_bf16 v[62:65], v[116:119], v[196:199], v[64:67]
	v_mfma_f32_16x16x32_bf16 v[66:69], v[124:127], v[196:199], v[68:71]
	v_mfma_f32_16x16x32_bf16 v[70:73], v[116:119], v[204:207], v[72:75]
	v_mfma_f32_16x16x32_bf16 v[74:77], v[124:127], v[204:207], v[76:79]
	v_mfma_f32_16x16x32_bf16 v[78:81], v[116:119], v[212:215], v[80:83]
	v_mfma_f32_16x16x32_bf16 v[82:85], v[124:127], v[212:215], v[84:87]
	v_mfma_f32_16x16x32_bf16 v[86:89], v[116:119], v[220:223], v[88:91]
	v_mfma_f32_16x16x32_bf16 v[90:93], v[124:127], v[220:223], v[92:95]
	v_mfma_f32_16x16x32_bf16 v[62:65], v[120:123], v[200:203], v[62:65]
	v_mfma_f32_16x16x32_bf16 v[66:69], v[152:155], v[200:203], v[66:69]
	v_mfma_f32_16x16x32_bf16 v[70:73], v[120:123], v[208:211], v[70:73]
	v_mfma_f32_16x16x32_bf16 v[74:77], v[152:155], v[208:211], v[74:77]
	v_mfma_f32_16x16x32_bf16 v[78:81], v[120:123], v[216:219], v[78:81]
	v_mfma_f32_16x16x32_bf16 v[82:85], v[152:155], v[216:219], v[82:85]
	v_mfma_f32_16x16x32_bf16 v[86:89], v[120:123], v[224:227], v[86:89]
	v_mfma_f32_16x16x32_bf16 v[90:93], v[152:155], v[224:227], v[90:93]
	s_setprio 0
	s_setprio 1
	v_mfma_f32_16x16x32_bf16 v[94:97], v[156:159], v[196:199], v[96:99]
	v_mfma_f32_16x16x32_bf16 v[98:101], v[188:191], v[196:199], v[100:103]
	v_mfma_f32_16x16x32_bf16 v[102:105], v[156:159], v[204:207], v[104:107]
	v_mfma_f32_16x16x32_bf16 v[38:41], v[188:191], v[204:207], v[38:41]
	v_mfma_f32_16x16x32_bf16 v[42:45], v[156:159], v[212:215], v[42:45]
	v_mfma_f32_16x16x32_bf16 v[46:49], v[188:191], v[212:215], v[46:49]
	v_mfma_f32_16x16x32_bf16 v[50:53], v[156:159], v[220:223], v[50:53]
	v_mfma_f32_16x16x32_bf16 v[54:57], v[188:191], v[220:223], v[54:57]
	v_mfma_f32_16x16x32_bf16 v[94:97], v[184:187], v[200:203], v[94:97]
	v_mfma_f32_16x16x32_bf16 v[98:101], v[192:195], v[200:203], v[98:101]
	v_mfma_f32_16x16x32_bf16 v[102:105], v[184:187], v[208:211], v[102:105]
	v_mfma_f32_16x16x32_bf16 v[38:41], v[192:195], v[208:211], v[38:41]
	v_mfma_f32_16x16x32_bf16 v[42:45], v[184:187], v[216:219], v[42:45]
	v_mfma_f32_16x16x32_bf16 v[46:49], v[192:195], v[216:219], v[46:49]
	v_mfma_f32_16x16x32_bf16 v[50:53], v[184:187], v[224:227], v[50:53]
	v_mfma_f32_16x16x32_bf16 v[54:57], v[192:195], v[224:227], v[54:57]
	s_setprio 0
.Lmsk_8:
	s_barrier
	s_mov_b32 m0, s70
	v_lshl_add_u64 v[106:107], v[0:1], 0, s[22:23]
	s_add_u32 s76, s38, 0x1a00
	ds_read_b128 v[196:199], v140 offset:16384
	ds_read_b128 v[200:203], v140 offset:17408
	ds_read_b128 v[204:207], v140 offset:18432
	ds_read_b128 v[208:211], v140 offset:19456
	ds_read_b128 v[212:215], v140 offset:20480
	ds_read_b128 v[216:219], v140 offset:21504
	ds_read_b128 v[220:223], v140 offset:22528
	ds_read_b128 v[224:227], v140 offset:23552
	global_load_lds_dwordx4 v[106:107], off
	v_lshl_add_u64 v[106:107], v[2:3], 0, s[22:23]
	s_mov_b32 m0, s67
	s_addc_u32 s77, s39, 0
	global_load_lds_dwordx4 v[106:107], off
	v_lshl_add_u64 v[106:107], s[76:77], 0, v[130:131]
	s_mov_b32 m0, s68
	s_nop 0
	global_load_lds_dwordx4 v[106:107], off
	v_lshl_add_u64 v[106:107], s[76:77], 0, v[134:135]
	s_mov_b32 m0, s69
	s_nop 0
	global_load_lds_dwordx4 v[106:107], off
	v_lshl_add_u64 v[106:107], v[4:5], 0, s[22:23]
	s_mov_b32 m0, s46
	s_nop 0
	global_load_lds_dwordx4 v[106:107], off
	v_lshl_add_u64 v[106:107], v[6:7], 0, s[22:23]
	s_mov_b32 m0, s47
	s_nop 0
	global_load_lds_dwordx4 v[106:107], off
	s_waitcnt vmcnt(8)
	s_waitcnt lgkmcnt(0)
	s_barrier
	s_cmp_le_i32 s51, s82
	s_cbranch_scc1 .Lmsk_7
	s_setprio 1
	s_waitcnt lgkmcnt(0)
	v_mfma_f32_16x16x32_bf16 v[10:13], v[116:119], v[220:223], v[10:13]
	v_mfma_f32_16x16x32_bf16 v[14:17], v[124:127], v[220:223], v[14:17]
	v_mfma_f32_16x16x32_bf16 v[160:163], v[116:119], v[196:199], v[160:163]
	v_mfma_f32_16x16x32_bf16 v[164:167], v[124:127], v[196:199], v[164:167]
	v_mfma_f32_16x16x32_bf16 v[168:171], v[116:119], v[204:207], v[168:171]
	v_mfma_f32_16x16x32_bf16 v[172:175], v[124:127], v[204:207], v[172:175]
	v_mfma_f32_16x16x32_bf16 v[176:179], v[116:119], v[212:215], v[176:179]
	v_mfma_f32_16x16x32_bf16 v[180:183], v[124:127], v[212:215], v[180:183]
	v_mfma_f32_16x16x32_bf16 v[10:13], v[120:123], v[224:227], v[10:13]
	v_mfma_f32_16x16x32_bf16 v[14:17], v[152:155], v[224:227], v[14:17]
	v_mfma_f32_16x16x32_bf16 v[160:163], v[120:123], v[200:203], v[160:163]
	v_mfma_f32_16x16x32_bf16 v[164:167], v[152:155], v[200:203], v[164:167]
	v_mfma_f32_16x16x32_bf16 v[168:171], v[120:123], v[208:211], v[168:171]
	v_mfma_f32_16x16x32_bf16 v[172:175], v[152:155], v[208:211], v[172:175]
	v_mfma_f32_16x16x32_bf16 v[176:179], v[120:123], v[216:219], v[176:179]
	v_mfma_f32_16x16x32_bf16 v[180:183], v[152:155], v[216:219], v[180:183]
	s_setprio 0
	s_setprio 1
	v_mfma_f32_16x16x32_bf16 v[18:21], v[156:159], v[196:199], v[18:21]
	v_mfma_f32_16x16x32_bf16 v[30:33], v[188:191], v[196:199], v[30:33]
	v_mfma_f32_16x16x32_bf16 v[34:37], v[156:159], v[204:207], v[34:37]
	v_mfma_f32_16x16x32_bf16 v[58:61], v[188:191], v[204:207], v[58:61]
	v_mfma_f32_16x16x32_bf16 v[106:109], v[156:159], v[212:215], v[108:111]
	v_mfma_f32_16x16x32_bf16 v[110:113], v[188:191], v[212:215], v[112:115]
	v_mfma_f32_16x16x32_bf16 v[22:25], v[156:159], v[220:223], v[22:25]
	v_mfma_f32_16x16x32_bf16 v[26:29], v[188:191], v[220:223], v[26:29]
	v_mfma_f32_16x16x32_bf16 v[18:21], v[184:187], v[200:203], v[18:21]
	v_mfma_f32_16x16x32_bf16 v[30:33], v[192:195], v[200:203], v[30:33]
	v_mfma_f32_16x16x32_bf16 v[34:37], v[184:187], v[208:211], v[34:37]
	v_mfma_f32_16x16x32_bf16 v[58:61], v[192:195], v[208:211], v[58:61]
	v_mfma_f32_16x16x32_bf16 v[106:109], v[184:187], v[216:219], v[106:109]
	v_mfma_f32_16x16x32_bf16 v[110:113], v[192:195], v[216:219], v[110:113]
	v_mfma_f32_16x16x32_bf16 v[22:25], v[184:187], v[224:227], v[22:25]
	v_mfma_f32_16x16x32_bf16 v[26:29], v[192:195], v[224:227], v[26:29]
	s_setprio 0
.Lmsk_7:
	s_barrier
	ds_read_b128 v[114:117], v8
	ds_read_b128 v[118:121], v8 offset:1024
	ds_read_b128 v[122:125], v8 offset:2048
	ds_read_b128 v[152:155], v8 offset:3072
	ds_read_b128 v[156:159], v9
	ds_read_b128 v[184:187], v9 offset:1024
	ds_read_b128 v[188:191], v9 offset:2048
	ds_read_b128 v[192:195], v9 offset:3072
	s_add_u32 s76, s36, 0x18200
	s_addc_u32 s77, s37, 0
	s_mov_b32 m0, s49
	v_lshl_add_u64 v[126:127], s[76:77], 0, v[128:129]
	ds_read_b128 v[196:199], v140 offset:32768
	ds_read_b128 v[200:203], v140 offset:33792
	ds_read_b128 v[204:207], v140 offset:34816
	ds_read_b128 v[208:211], v140 offset:35840
	ds_read_b128 v[212:215], v140 offset:36864
	ds_read_b128 v[216:219], v140 offset:37888
	ds_read_b128 v[220:223], v140 offset:38912
	ds_read_b128 v[224:227], v140 offset:39936
	global_load_lds_dwordx4 v[126:127], off
	v_lshl_add_u64 v[126:127], s[76:77], 0, v[132:133]
	s_mov_b32 m0, s50
	s_nop 0
	global_load_lds_dwordx4 v[126:127], off
	s_waitcnt vmcnt(8)
	s_waitcnt lgkmcnt(0)
	s_barrier
	s_cmp_le_i32 s51, s81
	s_cbranch_scc1 .Lmsk_6
	s_setprio 1
	s_waitcnt lgkmcnt(0)
	v_mfma_f32_16x16x32_bf16 v[62:65], v[114:117], v[196:199], v[62:65]
	v_mfma_f32_16x16x32_bf16 v[66:69], v[122:125], v[196:199], v[66:69]
	v_mfma_f32_16x16x32_bf16 v[70:73], v[114:117], v[204:207], v[70:73]
	v_mfma_f32_16x16x32_bf16 v[74:77], v[122:125], v[204:207], v[74:77]
	v_mfma_f32_16x16x32_bf16 v[78:81], v[114:117], v[212:215], v[78:81]
	v_mfma_f32_16x16x32_bf16 v[82:85], v[122:125], v[212:215], v[82:85]
	v_mfma_f32_16x16x32_bf16 v[86:89], v[114:117], v[220:223], v[86:89]
	v_mfma_f32_16x16x32_bf16 v[90:93], v[122:125], v[220:223], v[90:93]
	v_mfma_f32_16x16x32_bf16 v[62:65], v[118:121], v[200:203], v[62:65]
	v_mfma_f32_16x16x32_bf16 v[66:69], v[152:155], v[200:203], v[66:69]
	v_mfma_f32_16x16x32_bf16 v[70:73], v[118:121], v[208:211], v[70:73]
	v_mfma_f32_16x16x32_bf16 v[74:77], v[152:155], v[208:211], v[74:77]
	v_mfma_f32_16x16x32_bf16 v[78:81], v[118:121], v[216:219], v[78:81]
	v_mfma_f32_16x16x32_bf16 v[82:85], v[152:155], v[216:219], v[82:85]
	v_mfma_f32_16x16x32_bf16 v[86:89], v[118:121], v[224:227], v[86:89]
	v_mfma_f32_16x16x32_bf16 v[90:93], v[152:155], v[224:227], v[90:93]
	s_setprio 0
	s_setprio 1
	v_mfma_f32_16x16x32_bf16 v[94:97], v[156:159], v[196:199], v[94:97]
	v_mfma_f32_16x16x32_bf16 v[98:101], v[188:191], v[196:199], v[98:101]
	v_mfma_f32_16x16x32_bf16 v[102:105], v[156:159], v[204:207], v[102:105]
	v_mfma_f32_16x16x32_bf16 v[38:41], v[188:191], v[204:207], v[38:41]
	v_mfma_f32_16x16x32_bf16 v[42:45], v[156:159], v[212:215], v[42:45]
	v_mfma_f32_16x16x32_bf16 v[46:49], v[188:191], v[212:215], v[46:49]
	v_mfma_f32_16x16x32_bf16 v[50:53], v[156:159], v[220:223], v[50:53]
	v_mfma_f32_16x16x32_bf16 v[54:57], v[188:191], v[220:223], v[54:57]
	v_mfma_f32_16x16x32_bf16 v[94:97], v[184:187], v[200:203], v[94:97]
	v_mfma_f32_16x16x32_bf16 v[98:101], v[192:195], v[200:203], v[98:101]
	v_mfma_f32_16x16x32_bf16 v[102:105], v[184:187], v[208:211], v[102:105]
	v_mfma_f32_16x16x32_bf16 v[38:41], v[192:195], v[208:211], v[38:41]
	v_mfma_f32_16x16x32_bf16 v[42:45], v[184:187], v[216:219], v[42:45]
	v_mfma_f32_16x16x32_bf16 v[46:49], v[192:195], v[216:219], v[46:49]
	v_mfma_f32_16x16x32_bf16 v[50:53], v[184:187], v[224:227], v[50:53]
	v_mfma_f32_16x16x32_bf16 v[54:57], v[192:195], v[224:227], v[54:57]
	s_setprio 0
.Lmsk_6:
	s_barrier
	s_mov_b32 m0, s74
	v_lshl_add_u64 v[0:1], v[0:1], 0, s[24:25]
	s_add_u32 s38, s38, 0x1a80
	ds_read_b128 v[196:199], v140 offset:49152
	ds_read_b128 v[200:203], v140 offset:50176
	ds_read_b128 v[204:207], v140 offset:51200
	ds_read_b128 v[208:211], v140 offset:52224
	ds_read_b128 v[212:215], v140 offset:53248
	ds_read_b128 v[216:219], v140 offset:54272
	ds_read_b128 v[220:223], v140 offset:55296
	ds_read_b128 v[224:227], v140 offset:56320
	global_load_lds_dwordx4 v[0:1], off
	v_lshl_add_u64 v[0:1], v[2:3], 0, s[24:25]
	s_mov_b32 m0, s71
	s_addc_u32 s39, s39, 0
	global_load_lds_dwordx4 v[0:1], off
	v_lshl_add_u64 v[0:1], s[38:39], 0, v[130:131]
	s_mov_b32 m0, s72
	s_nop 0
	global_load_lds_dwordx4 v[0:1], off
	v_lshl_add_u64 v[0:1], s[38:39], 0, v[134:135]
	s_mov_b32 m0, s73
	s_nop 0
	global_load_lds_dwordx4 v[0:1], off
	v_lshl_add_u64 v[0:1], v[4:5], 0, s[24:25]
	s_mov_b32 m0, s52
	s_nop 0
	global_load_lds_dwordx4 v[0:1], off
	v_lshl_add_u64 v[0:1], v[6:7], 0, s[24:25]
	s_mov_b32 m0, s53
	s_nop 0
	global_load_lds_dwordx4 v[0:1], off
	s_waitcnt vmcnt(8)
	s_waitcnt lgkmcnt(0)
	s_barrier
	s_cmp_le_i32 s51, s82
	s_cbranch_scc1 .Lmsk_5
	s_setprio 1
	s_waitcnt lgkmcnt(0)
	v_mfma_f32_16x16x32_bf16 v[0:3], v[114:117], v[196:199], v[160:163]
	v_mfma_f32_16x16x32_bf16 v[4:7], v[122:125], v[196:199], v[164:167]
	v_mfma_f32_16x16x32_bf16 v[10:13], v[114:117], v[220:223], v[10:13]
	v_mfma_f32_16x16x32_bf16 v[14:17], v[122:125], v[220:223], v[14:17]
	v_mfma_f32_16x16x32_bf16 v[0:3], v[118:121], v[200:203], v[0:3]
	v_mfma_f32_16x16x32_bf16 v[4:7], v[152:155], v[200:203], v[4:7]
	v_mfma_f32_16x16x32_bf16 v[160:163], v[114:117], v[204:207], v[168:171]
	v_mfma_f32_16x16x32_bf16 v[164:167], v[122:125], v[204:207], v[172:175]
	v_mfma_f32_16x16x32_bf16 v[168:171], v[114:117], v[212:215], v[176:179]
	v_mfma_f32_16x16x32_bf16 v[172:175], v[122:125], v[212:215], v[180:183]
	v_mfma_f32_16x16x32_bf16 v[10:13], v[118:121], v[224:227], v[10:13]
	v_mfma_f32_16x16x32_bf16 v[14:17], v[152:155], v[224:227], v[14:17]
	v_mfma_f32_16x16x32_bf16 v[160:163], v[118:121], v[208:211], v[160:163]
	v_mfma_f32_16x16x32_bf16 v[164:167], v[152:155], v[208:211], v[164:167]
	v_mfma_f32_16x16x32_bf16 v[168:171], v[118:121], v[216:219], v[168:171]
	v_mfma_f32_16x16x32_bf16 v[172:175], v[152:155], v[216:219], v[172:175]
	s_setprio 0
	s_setprio 1
	v_mfma_f32_16x16x32_bf16 v[18:21], v[156:159], v[196:199], v[18:21]
	v_mfma_f32_16x16x32_bf16 v[30:33], v[188:191], v[196:199], v[30:33]
	v_mfma_f32_16x16x32_bf16 v[34:37], v[156:159], v[204:207], v[34:37]
	v_mfma_f32_16x16x32_bf16 v[58:61], v[188:191], v[204:207], v[58:61]
	v_mfma_f32_16x16x32_bf16 v[106:109], v[156:159], v[212:215], v[106:109]
	v_mfma_f32_16x16x32_bf16 v[110:113], v[188:191], v[212:215], v[110:113]
	v_mfma_f32_16x16x32_bf16 v[22:25], v[156:159], v[220:223], v[22:25]
	v_mfma_f32_16x16x32_bf16 v[26:29], v[188:191], v[220:223], v[26:29]
	v_mfma_f32_16x16x32_bf16 v[18:21], v[184:187], v[200:203], v[18:21]
	v_mfma_f32_16x16x32_bf16 v[30:33], v[192:195], v[200:203], v[30:33]
	v_mfma_f32_16x16x32_bf16 v[34:37], v[184:187], v[208:211], v[34:37]
	v_mfma_f32_16x16x32_bf16 v[58:61], v[192:195], v[208:211], v[58:61]
	v_mfma_f32_16x16x32_bf16 v[106:109], v[184:187], v[216:219], v[106:109]
	v_mfma_f32_16x16x32_bf16 v[110:113], v[192:195], v[216:219], v[110:113]
	v_mfma_f32_16x16x32_bf16 v[22:25], v[184:187], v[224:227], v[22:25]
	v_mfma_f32_16x16x32_bf16 v[26:29], v[192:195], v[224:227], v[26:29]
	s_setprio 0
.Lmsk_5:
	s_barrier
	ds_read_b128 v[114:117], v149
	ds_read_b128 v[118:121], v149 offset:1024
	ds_read_b128 v[122:125], v149 offset:2048
	ds_read_b128 v[152:155], v149 offset:3072
	ds_read_b128 v[156:159], v150
	ds_read_b128 v[176:179], v150 offset:1024
	ds_read_b128 v[180:183], v150 offset:2048
	ds_read_b128 v[184:187], v150 offset:3072
	s_add_u32 s36, s36, 0x18280
	s_addc_u32 s37, s37, 0
	s_mov_b32 m0, s61
	v_lshl_add_u64 v[126:127], s[36:37], 0, v[128:129]
	ds_read_b128 v[188:191], v140
	ds_read_b128 v[192:195], v140 offset:1024
	ds_read_b128 v[196:199], v140 offset:2048
	ds_read_b128 v[200:203], v140 offset:3072
	ds_read_b128 v[204:207], v140 offset:4096
	ds_read_b128 v[208:211], v140 offset:5120
	ds_read_b128 v[212:215], v140 offset:6144
	ds_read_b128 v[216:219], v140 offset:7168
	global_load_lds_dwordx4 v[126:127], off
	v_lshl_add_u64 v[126:127], s[36:37], 0, v[132:133]
	s_mov_b32 m0, s62
	s_nop 0
	global_load_lds_dwordx4 v[126:127], off
	s_waitcnt vmcnt(8)
	s_waitcnt lgkmcnt(0)
	s_barrier
	s_cmp_le_i32 s51, s81
	s_cbranch_scc1 .Lmsk_4
	s_setprio 1
	s_waitcnt lgkmcnt(0)
	v_mfma_f32_16x16x32_bf16 v[82:85], v[122:125], v[204:207], v[82:85]
	v_mfma_f32_16x16x32_bf16 v[220:223], v[152:155], v[208:211], v[82:85]
	v_mfma_f32_16x16x32_bf16 v[82:85], v[114:117], v[212:215], v[86:89]
	v_mfma_f32_16x16x32_bf16 v[62:65], v[114:117], v[188:191], v[62:65]
	v_mfma_f32_16x16x32_bf16 v[66:69], v[122:125], v[188:191], v[66:69]
	v_mfma_f32_16x16x32_bf16 v[70:73], v[114:117], v[196:199], v[70:73]
	v_mfma_f32_16x16x32_bf16 v[74:77], v[122:125], v[196:199], v[74:77]
	v_mfma_f32_16x16x32_bf16 v[78:81], v[114:117], v[204:207], v[78:81]
	v_mfma_f32_16x16x32_bf16 v[224:227], v[118:121], v[216:219], v[82:85]
	v_mfma_f32_16x16x32_bf16 v[82:85], v[122:125], v[212:215], v[90:93]
	v_mfma_f32_16x16x32_bf16 v[62:65], v[118:121], v[192:195], v[62:65]
	v_mfma_f32_16x16x32_bf16 v[66:69], v[152:155], v[192:195], v[66:69]
	v_mfma_f32_16x16x32_bf16 v[70:73], v[118:121], v[200:203], v[70:73]
	v_mfma_f32_16x16x32_bf16 v[74:77], v[152:155], v[200:203], v[74:77]
	v_mfma_f32_16x16x32_bf16 v[78:81], v[118:121], v[208:211], v[78:81]
	v_mfma_f32_16x16x32_bf16 v[88:91], v[152:155], v[216:219], v[82:85]
	s_setprio 0
	s_setprio 1
	v_mfma_f32_16x16x32_bf16 v[82:85], v[156:159], v[188:191], v[94:97]
	v_mfma_f32_16x16x32_bf16 v[92:95], v[176:179], v[192:195], v[82:85]
	v_mfma_f32_16x16x32_bf16 v[82:85], v[180:183], v[188:191], v[98:101]
	v_mfma_f32_16x16x32_bf16 v[38:41], v[180:183], v[196:199], v[38:41]
	v_mfma_f32_16x16x32_bf16 v[42:45], v[156:159], v[204:207], v[42:45]
	v_mfma_f32_16x16x32_bf16 v[46:49], v[180:183], v[204:207], v[46:49]
	v_mfma_f32_16x16x32_bf16 v[50:53], v[156:159], v[212:215], v[50:53]
	v_mfma_f32_16x16x32_bf16 v[54:57], v[180:183], v[212:215], v[54:57]
	v_mfma_f32_16x16x32_bf16 v[188:191], v[184:187], v[192:195], v[82:85]
	v_mfma_f32_16x16x32_bf16 v[82:85], v[156:159], v[196:199], v[102:105]
	v_mfma_f32_16x16x32_bf16 v[38:41], v[184:187], v[200:203], v[38:41]
	v_mfma_f32_16x16x32_bf16 v[42:45], v[176:179], v[208:211], v[42:45]
	v_mfma_f32_16x16x32_bf16 v[46:49], v[184:187], v[208:211], v[46:49]
	v_mfma_f32_16x16x32_bf16 v[50:53], v[176:179], v[216:219], v[50:53]
	v_mfma_f32_16x16x32_bf16 v[54:57], v[184:187], v[216:219], v[54:57]
	v_mfma_f32_16x16x32_bf16 v[192:195], v[176:179], v[200:203], v[82:85]
	s_setprio 0
.Lmsk_4:
	s_barrier
	s_mov_b32 m0, s70
	v_lshl_add_u64 v[136:137], s[28:29], 0, v[130:131]
	s_add_u32 s36, s28, 0x1800
	ds_read_b128 v[82:85], v140 offset:16384
	ds_read_b128 v[96:99], v140 offset:17408
	ds_read_b128 v[100:103], v140 offset:18432
	ds_read_b128 v[196:199], v140 offset:19456
	ds_read_b128 v[200:203], v140 offset:20480
	ds_read_b128 v[204:207], v140 offset:21504
	ds_read_b128 v[208:211], v140 offset:22528
	ds_read_b128 v[212:215], v140 offset:23552
	global_load_lds_dwordx4 v[136:137], off
	v_lshl_add_u64 v[142:143], s[28:29], 0, v[134:135]
	s_mov_b32 m0, s67
	s_addc_u32 s37, s29, 0
	global_load_lds_dwordx4 v[142:143], off
	v_lshl_add_u64 v[86:87], s[36:37], 0, v[130:131]
	s_mov_b32 m0, s68
	v_lshl_add_u64 v[144:145], s[26:27], 0, v[128:129]
	global_load_lds_dwordx4 v[86:87], off
	v_lshl_add_u64 v[86:87], s[36:37], 0, v[134:135]
	s_mov_b32 m0, s69
	v_lshl_add_u64 v[146:147], s[26:27], 0, v[132:133]
	global_load_lds_dwordx4 v[86:87], off
	s_mov_b32 m0, s46
	s_nop 0
	global_load_lds_dwordx4 v[144:145], off
	s_mov_b32 m0, s47
	s_nop 0
	global_load_lds_dwordx4 v[146:147], off
	s_waitcnt vmcnt(8)
	s_waitcnt lgkmcnt(0)
	s_barrier
	s_cmp_le_i32 s51, s82
	s_cbranch_scc1 .Lmsk_3
	s_setprio 1
	s_waitcnt lgkmcnt(0)
	v_mfma_f32_16x16x32_bf16 v[0:3], v[114:117], v[82:85], v[0:3]
	v_mfma_f32_16x16x32_bf16 v[4:7], v[122:125], v[82:85], v[4:7]
	v_mfma_f32_16x16x32_bf16 v[10:13], v[114:117], v[208:211], v[10:13]
	v_mfma_f32_16x16x32_bf16 v[0:3], v[118:121], v[96:99], v[0:3]
	v_mfma_f32_16x16x32_bf16 v[4:7], v[152:155], v[96:99], v[4:7]
	v_mfma_f32_16x16x32_bf16 v[160:163], v[114:117], v[100:103], v[160:163]
	v_mfma_f32_16x16x32_bf16 v[164:167], v[122:125], v[100:103], v[164:167]
	v_mfma_f32_16x16x32_bf16 v[168:171], v[114:117], v[200:203], v[168:171]
	v_mfma_f32_16x16x32_bf16 v[172:175], v[122:125], v[200:203], v[172:175]
	v_mfma_f32_16x16x32_bf16 v[10:13], v[118:121], v[212:215], v[10:13]
	v_mfma_f32_16x16x32_bf16 v[14:17], v[122:125], v[208:211], v[14:17]
	v_mfma_f32_16x16x32_bf16 v[160:163], v[118:121], v[196:199], v[160:163]
	v_mfma_f32_16x16x32_bf16 v[164:167], v[152:155], v[196:199], v[164:167]
	v_mfma_f32_16x16x32_bf16 v[168:171], v[118:121], v[204:207], v[168:171]
	v_mfma_f32_16x16x32_bf16 v[172:175], v[152:155], v[204:207], v[172:175]
	v_mfma_f32_16x16x32_bf16 v[152:155], v[152:155], v[212:215], v[14:17]
	s_setprio 0
	s_setprio 1
	v_mfma_f32_16x16x32_bf16 v[14:17], v[156:159], v[82:85], v[18:21]
	v_mfma_f32_16x16x32_bf16 v[216:219], v[176:179], v[96:99], v[14:17]
	v_mfma_f32_16x16x32_bf16 v[14:17], v[180:183], v[82:85], v[30:33]
	v_mfma_f32_16x16x32_bf16 v[228:231], v[184:187], v[96:99], v[14:17]
	v_mfma_f32_16x16x32_bf16 v[14:17], v[156:159], v[100:103], v[34:37]
	v_mfma_f32_16x16x32_bf16 v[232:235], v[176:179], v[196:199], v[14:17]
	v_mfma_f32_16x16x32_bf16 v[14:17], v[180:183], v[100:103], v[58:61]
	v_mfma_f32_16x16x32_bf16 v[196:199], v[184:187], v[196:199], v[14:17]
	v_mfma_f32_16x16x32_bf16 v[14:17], v[156:159], v[200:203], v[106:109]
	v_mfma_f32_16x16x32_bf16 v[236:239], v[176:179], v[204:207], v[14:17]
	v_mfma_f32_16x16x32_bf16 v[14:17], v[180:183], v[200:203], v[110:113]
	v_mfma_f32_16x16x32_bf16 v[200:203], v[184:187], v[204:207], v[14:17]
	v_mfma_f32_16x16x32_bf16 v[14:17], v[156:159], v[208:211], v[22:25]
	v_mfma_f32_16x16x32_bf16 v[156:159], v[176:179], v[212:215], v[14:17]
	v_mfma_f32_16x16x32_bf16 v[14:17], v[180:183], v[208:211], v[26:29]
	v_mfma_f32_16x16x32_bf16 v[176:179], v[184:187], v[212:215], v[14:17]
	s_setprio 0
.Lmsk_3:
	s_barrier
	ds_read_b128 v[24:27], v8
	ds_read_b128 v[28:31], v8 offset:1024
	ds_read_b128 v[58:61], v8 offset:2048
	ds_read_b128 v[180:183], v8 offset:3072
	ds_read_b128 v[184:187], v9
	ds_read_b128 v[204:207], v9 offset:1024
	ds_read_b128 v[208:211], v9 offset:2048
	ds_read_b128 v[212:215], v9 offset:3072
	s_add_u32 s36, s26, 0x18000
	s_addc_u32 s37, s27, 0
	s_mov_b32 m0, s49
	v_lshl_add_u64 v[8:9], s[36:37], 0, v[128:129]
	ds_read_b128 v[14:17], v140 offset:32768
	ds_read_b128 v[18:21], v140 offset:33792
	ds_read_b128 v[32:35], v140 offset:34816
	ds_read_b128 v[108:111], v140 offset:35840
	ds_read_b128 v[240:243], v140 offset:36864
	ds_read_b128 v[244:247], v140 offset:37888
	ds_read_b128 v[248:251], v140 offset:38912
	ds_read_b128 v[252:255], v140 offset:39936
	global_load_lds_dwordx4 v[8:9], off
	v_lshl_add_u64 v[8:9], s[36:37], 0, v[132:133]
	s_mov_b32 m0, s50
	s_nop 0
	global_load_lds_dwordx4 v[8:9], off
	s_waitcnt vmcnt(8)
	s_waitcnt lgkmcnt(0)
	s_barrier
	s_cmp_le_i32 s51, s81
	s_cbranch_scc1 .Lmsk_2
	s_setprio 1
	s_waitcnt lgkmcnt(0)
	v_mfma_f32_16x16x32_bf16 v[62:65], v[24:27], v[14:17], v[62:65]
	v_mfma_f32_16x16x32_bf16 v[112:115], v[28:31], v[18:21], v[62:65]
	v_mfma_f32_16x16x32_bf16 v[62:65], v[58:61], v[14:17], v[66:69]
	v_mfma_f32_16x16x32_bf16 v[116:119], v[180:183], v[18:21], v[62:65]
	v_mfma_f32_16x16x32_bf16 v[62:65], v[24:27], v[32:35], v[70:73]
	v_mfma_f32_16x16x32_bf16 v[96:99], v[28:31], v[108:111], v[62:65]
	v_mfma_f32_16x16x32_bf16 v[62:65], v[58:61], v[32:35], v[74:77]
	v_mfma_f32_16x16x32_bf16 v[100:103], v[180:183], v[108:111], v[62:65]
	v_mfma_f32_16x16x32_bf16 v[62:65], v[24:27], v[240:243], v[78:81]
	v_mfma_f32_16x16x32_bf16 v[80:83], v[28:31], v[244:247], v[62:65]
	v_mfma_f32_16x16x32_bf16 v[62:65], v[58:61], v[240:243], v[220:223]
	v_mfma_f32_16x16x32_bf16 v[84:87], v[180:183], v[244:247], v[62:65]
	v_mfma_f32_16x16x32_bf16 v[62:65], v[24:27], v[248:251], v[224:227]
	v_mfma_f32_16x16x32_bf16 v[68:71], v[58:61], v[248:251], v[88:91]
	v_mfma_f32_16x16x32_bf16 v[64:67], v[28:31], v[252:255], v[62:65]
	v_mfma_f32_16x16x32_bf16 v[68:71], v[180:183], v[252:255], v[68:71]
	s_setprio 0
	s_setprio 1
	v_mfma_f32_16x16x32_bf16 v[72:75], v[184:187], v[14:17], v[92:95]
	v_mfma_f32_16x16x32_bf16 v[14:17], v[208:211], v[14:17], v[188:191]
	v_mfma_f32_16x16x32_bf16 v[124:127], v[212:215], v[18:21], v[14:17]
	v_mfma_f32_16x16x32_bf16 v[14:17], v[184:187], v[32:35], v[192:195]
	v_mfma_f32_16x16x32_bf16 v[104:107], v[204:207], v[108:111], v[14:17]
	v_mfma_f32_16x16x32_bf16 v[14:17], v[208:211], v[32:35], v[38:41]
	v_mfma_f32_16x16x32_bf16 v[108:111], v[212:215], v[108:111], v[14:17]
	v_mfma_f32_16x16x32_bf16 v[14:17], v[184:187], v[240:243], v[42:45]
	v_mfma_f32_16x16x32_bf16 v[88:91], v[204:207], v[244:247], v[14:17]
	v_mfma_f32_16x16x32_bf16 v[14:17], v[208:211], v[240:243], v[46:49]
	v_mfma_f32_16x16x32_bf16 v[92:95], v[212:215], v[244:247], v[14:17]
	v_mfma_f32_16x16x32_bf16 v[14:17], v[184:187], v[248:251], v[50:53]
	v_mfma_f32_16x16x32_bf16 v[120:123], v[204:207], v[18:21], v[72:75]
	v_mfma_f32_16x16x32_bf16 v[72:75], v[204:207], v[252:255], v[14:17]
	v_mfma_f32_16x16x32_bf16 v[14:17], v[208:211], v[248:251], v[54:57]
	v_mfma_f32_16x16x32_bf16 v[76:79], v[212:215], v[252:255], v[14:17]
	s_setprio 0
.Lmsk_2:
	s_barrier
	s_mov_b32 m0, s74
	v_lshl_add_u64 v[8:9], v[136:137], 0, s[14:15]
	s_add_u32 s36, s28, 0x1880
	ds_read_b128 v[40:43], v140 offset:49152
	ds_read_b128 v[44:47], v140 offset:50176
	ds_read_b128 v[188:191], v140 offset:51200
	ds_read_b128 v[192:195], v140 offset:52224
	ds_read_b128 v[220:223], v140 offset:53248
	ds_read_b128 v[224:227], v140 offset:54272
	ds_read_b128 v[240:243], v140 offset:55296
	ds_read_b128 v[244:247], v140 offset:56320
	global_load_lds_dwordx4 v[8:9], off
	v_lshl_add_u64 v[8:9], v[142:143], 0, s[14:15]
	s_mov_b32 m0, s71
	s_addc_u32 s37, s29, 0
	global_load_lds_dwordx4 v[8:9], off
	v_lshl_add_u64 v[8:9], s[36:37], 0, v[130:131]
	s_mov_b32 m0, s72
	s_nop 0
	global_load_lds_dwordx4 v[8:9], off
	v_lshl_add_u64 v[8:9], s[36:37], 0, v[134:135]
	s_mov_b32 m0, s73
	s_nop 0
	global_load_lds_dwordx4 v[8:9], off
	v_lshl_add_u64 v[8:9], v[144:145], 0, s[14:15]
	s_mov_b32 m0, s52
	s_nop 0
	global_load_lds_dwordx4 v[8:9], off
	v_lshl_add_u64 v[8:9], v[146:147], 0, s[14:15]
	s_mov_b32 m0, s53
	s_nop 0
	global_load_lds_dwordx4 v[8:9], off
	s_waitcnt vmcnt(8)
	s_waitcnt lgkmcnt(0)
	s_barrier
	s_cmp_le_i32 s51, s82
	s_cbranch_scc1 .Lmsk_1
	s_setprio 1
	s_waitcnt lgkmcnt(0)
	v_mfma_f32_16x16x32_bf16 v[0:3], v[24:27], v[40:43], v[0:3]
	v_mfma_f32_16x16x32_bf16 v[48:51], v[28:31], v[44:47], v[0:3]
	v_mfma_f32_16x16x32_bf16 v[0:3], v[58:61], v[40:43], v[4:7]
	v_mfma_f32_16x16x32_bf16 v[52:55], v[180:183], v[44:47], v[0:3]
	v_mfma_f32_16x16x32_bf16 v[0:3], v[24:27], v[188:191], v[160:163]
	v_mfma_f32_16x16x32_bf16 v[32:35], v[28:31], v[192:195], v[0:3]
	v_mfma_f32_16x16x32_bf16 v[0:3], v[58:61], v[188:191], v[164:167]
	v_mfma_f32_16x16x32_bf16 v[36:39], v[180:183], v[192:195], v[0:3]
	v_mfma_f32_16x16x32_bf16 v[0:3], v[24:27], v[220:223], v[168:171]
	v_mfma_f32_16x16x32_bf16 v[16:19], v[28:31], v[224:227], v[0:3]
	v_mfma_f32_16x16x32_bf16 v[0:3], v[58:61], v[220:223], v[172:175]
	v_mfma_f32_16x16x32_bf16 v[20:23], v[180:183], v[224:227], v[0:3]
	v_mfma_f32_16x16x32_bf16 v[0:3], v[24:27], v[240:243], v[10:13]
	v_mfma_f32_16x16x32_bf16 v[4:7], v[58:61], v[240:243], v[152:155]
	v_mfma_f32_16x16x32_bf16 v[0:3], v[28:31], v[244:247], v[0:3]
	v_mfma_f32_16x16x32_bf16 v[4:7], v[180:183], v[244:247], v[4:7]
	s_setprio 0
	s_setprio 1
	v_mfma_f32_16x16x32_bf16 v[8:11], v[184:187], v[40:43], v[216:219]
	v_mfma_f32_16x16x32_bf16 v[56:59], v[204:207], v[44:47], v[8:11]
	v_mfma_f32_16x16x32_bf16 v[8:11], v[208:211], v[40:43], v[228:231]
	v_mfma_f32_16x16x32_bf16 v[60:63], v[212:215], v[44:47], v[8:11]
	v_mfma_f32_16x16x32_bf16 v[8:11], v[184:187], v[188:191], v[232:235]
	v_mfma_f32_16x16x32_bf16 v[40:43], v[204:207], v[192:195], v[8:11]
	v_mfma_f32_16x16x32_bf16 v[8:11], v[208:211], v[188:191], v[196:199]
	v_mfma_f32_16x16x32_bf16 v[44:47], v[212:215], v[192:195], v[8:11]
	v_mfma_f32_16x16x32_bf16 v[8:11], v[184:187], v[220:223], v[236:239]
	v_mfma_f32_16x16x32_bf16 v[24:27], v[204:207], v[224:227], v[8:11]
	v_mfma_f32_16x16x32_bf16 v[8:11], v[208:211], v[220:223], v[200:203]
	v_mfma_f32_16x16x32_bf16 v[28:31], v[212:215], v[224:227], v[8:11]
	v_mfma_f32_16x16x32_bf16 v[8:11], v[184:187], v[240:243], v[156:159]
	v_mfma_f32_16x16x32_bf16 v[12:15], v[208:211], v[240:243], v[176:179]
	v_mfma_f32_16x16x32_bf16 v[8:11], v[204:207], v[244:247], v[8:11]
	v_mfma_f32_16x16x32_bf16 v[12:15], v[212:215], v[244:247], v[12:15]
	s_setprio 0
